# expert weight f32->fp8 conversion (w_gate_up, w_down) moved from the prologue phase into the attention phase: one 64x64 tile per wave per attention unit, loads overlapped with K/V staging
# speedup vs baseline: 1.0497x; 1.0350x over previous
.LBB0_15:
	s_or_b64 exec, exec, s[6:7]
	s_ashr_i32 s0, s2, 6
	v_readlane_b32 s1, v239, 23
	s_add_i32 s3, s0, s1
	v_readlane_b32 s38, v239, 11
	v_readlane_b32 s39, v239, 12
	v_readlane_b32 s40, v239, 15
	v_readlane_b32 s41, v239, 16
	v_and_b32_e32 v20, 63, v2
	v_lshlrev_b32_e32 v1, 2, v20
	v_and_b32_e32 v100, 60, v20
	v_and_b32_e32 v101, 3, v20
	v_lshlrev_b32_e32 v101, 4, v101
	s_mov_b32 s42, 0xaaaaaaaa
	s_mov_b32 s43, 0xaaaaaaaa
	s_mov_b32 s44, 0x55555555
	s_mov_b32 s45, 0x55555555
	s_mov_b32 s46, 0xcccccccc
	s_mov_b32 s47, 0xcccccccc
	s_mov_b32 s48, 0x33333333
	s_mov_b32 s49, 0x33333333
	s_mov_b32 s19, 0
.Lp0w_loop:
	s_cmp_gt_u32 s3, 2047
	s_cbranch_scc1 .LBB0_50
	s_mov_b32 s13, s3
	s_cmp_lt_u32 s13, 1472
	s_cbranch_scc0 .Lp0w_t1
	s_mul_i32 s14, s13, 45591
	s_lshr_b32 s14, s14, 22
	s_mul_i32 s15, s14, 92
	s_sub_i32 s15, s13, s15
	s_mul_i32 s16, s14, 1507328
	s_lshl_b32 s0, s15, 8
	s_add_i32 s16, s16, s0
	s_lshl_b32 s17, s15, 16
	s_lshl_b32 s0, s14, 6
	s_add_i32 s17, s17, s0
	s_add_i32 s17, s17, 0x200000
	s_mov_b64 s[36:37], s[82:83]
	s_mov_b32 s8, 23552
	s_movk_i32 s12, 1024
	s_branch .Lp0w_plain
.Lp0w_t1:
	s_sub_i32 s13, s13, 1472
	s_cmp_lt_u32 s13, 256
	s_cbranch_scc0 .Lp0w_t2
	s_lshr_b32 s14, s13, 4
	s_and_b32 s15, s13, 15
	s_lshl_b32 s16, s14, 18
	s_lshl_b32 s0, s15, 8
	s_add_i32 s16, s16, s0
	s_mul_i32 s17, s15, 81920
	s_lshl_b32 s0, s14, 6
	s_add_i32 s17, s17, s0
	s_add_i32 s17, s17, 0xe00000
	s_mov_b64 s[36:37], s[86:87]
	s_movk_i32 s8, 4096
	s_movk_i32 s12, 1280
	s_branch .Lp0w_plain
.Lp0w_t2:
	s_sub_i32 s13, s13, 256
	s_cmp_lt_u32 s13, 64
	s_cbranch_scc0 .Lp0w_t3
	s_lshr_b32 s14, s13, 4
	s_and_b32 s15, s13, 15
	s_lshl_b32 s16, s14, 18
	s_lshl_b32 s0, s15, 8
	s_add_i32 s16, s16, s0
	s_mul_i32 s17, s15, 81920
	s_lshl_b32 s0, s14, 6
	s_add_i32 s17, s17, s0
	s_add_i32 s17, s17, 0xe00400
	s_mov_b64 s[36:37], s[88:89]
	s_movk_i32 s8, 4096
	s_movk_i32 s12, 1280
	s_branch .Lp0w_plain
.Lp0w_t3:
	s_sub_i32 s13, s13, 64
	s_cmp_lt_u32 s13, 256
	s_cbranch_scc0 .Lp0w_t4
	s_lshr_b32 s14, s13, 4
	s_and_b32 s15, s13, 15
	s_lshl_b32 s16, s14, 18
	s_lshl_b32 s0, s15, 8
	s_add_i32 s16, s16, s0
	s_lshl_b32 s17, s15, 16
	s_lshl_b32 s0, s14, 6
	s_add_i32 s17, s17, s0
	s_add_i32 s17, s17, 0x1100000
	s_mov_b64 s[36:37], s[90:91]
	s_movk_i32 s8, 4096
	s_movk_i32 s12, 1024
	s_branch .Lp0w_plain
.Lp0w_t4:
	s_sub_i32 s13, s13, 256
	s_cmp_lt_u32 s13, 16384
	s_cbranch_scc0 .Lp0w_t5
	s_lshr_b32 s18, s13, 9
	s_bfe_u32 s14, s13, 0x40005
	s_and_b32 s15, s13, 31
	s_lshl_b32 s16, s18, 23
	s_lshl_b32 s0, s14, 19
	s_add_i32 s16, s16, s0
	s_lshl_b32 s0, s15, 8
	s_add_i32 s16, s16, s0
	s_lshl_b32 s17, s18, 11
	s_bfe_u32 s0, s15, 0x30001
	s_lshl_b32 s0, s0, 8
	s_add_i32 s17, s17, s0
	s_lshr_b32 s0, s15, 4
	s_lshl_b32 s0, s0, 7
	s_add_i32 s17, s17, s0
	s_and_b32 s0, s15, 1
	s_lshl_b32 s0, s0, 6
	s_add_i32 s17, s17, s0
	s_lshl_b32 s17, s17, 10
	s_lshl_b32 s0, s14, 6
	s_add_i32 s17, s17, s0
	s_add_i32 s17, s17, 0x2000000
	s_mov_b64 s[36:37], s[38:39]
	s_movk_i32 s8, 8192
	s_movk_i32 s12, 1024
	s_branch .Lp0w_nt
.Lp0w_t5:
	s_sub_i32 s13, s13, 16384
	s_lshr_b32 s18, s13, 8
	s_bfe_u32 s14, s13, 0x40004
	s_and_b32 s15, s13, 15
	s_lshl_b32 s16, s18, 22
	s_lshl_b32 s0, s14, 18
	s_add_i32 s16, s16, s0
	s_lshl_b32 s0, s15, 8
	s_add_i32 s16, s16, s0
	s_lshl_b32 s17, s18, 20
	s_lshl_b32 s0, s15, 16
	s_add_i32 s17, s17, s0
	s_lshl_b32 s0, s14, 6
	s_add_i32 s17, s17, s0
	s_add_i32 s17, s17, 0x6000000
	s_mov_b64 s[36:37], s[40:41]
	s_movk_i32 s8, 4096
	s_movk_i32 s12, 1024
.Lp0w_nt:
	s_add_u32 s6, s36, s16
	s_addc_u32 s7, s37, 0
	s_add_u32 s10, s62, s17
	s_addc_u32 s11, s63, 0
	v_mad_u32_u24 v3, v100, s12, v101
	v_add_u32_e32 v21, s12, v3
	v_add_u32_e32 v22, s12, v21
	v_add_u32_e32 v23, s12, v22
	global_load_dword v32, v1, s[6:7] nt
	s_add_u32 s6, s6, s8
	s_addc_u32 s7, s7, 0
	global_load_dword v33, v1, s[6:7] nt
	s_add_u32 s6, s6, s8
	s_addc_u32 s7, s7, 0
	global_load_dword v34, v1, s[6:7] nt
	s_add_u32 s6, s6, s8
	s_addc_u32 s7, s7, 0
	global_load_dword v35, v1, s[6:7] nt
	s_add_u32 s6, s6, s8
	s_addc_u32 s7, s7, 0
	global_load_dword v36, v1, s[6:7] nt
	s_add_u32 s6, s6, s8
	s_addc_u32 s7, s7, 0
	global_load_dword v37, v1, s[6:7] nt
	s_add_u32 s6, s6, s8
	s_addc_u32 s7, s7, 0
	global_load_dword v38, v1, s[6:7] nt
	s_add_u32 s6, s6, s8
	s_addc_u32 s7, s7, 0
	global_load_dword v39, v1, s[6:7] nt
	s_add_u32 s6, s6, s8
	s_addc_u32 s7, s7, 0
	global_load_dword v40, v1, s[6:7] nt
	s_add_u32 s6, s6, s8
	s_addc_u32 s7, s7, 0
	global_load_dword v41, v1, s[6:7] nt
	s_add_u32 s6, s6, s8
	s_addc_u32 s7, s7, 0
	global_load_dword v42, v1, s[6:7] nt
	s_add_u32 s6, s6, s8
	s_addc_u32 s7, s7, 0
	global_load_dword v43, v1, s[6:7] nt
	s_add_u32 s6, s6, s8
	s_addc_u32 s7, s7, 0
	global_load_dword v44, v1, s[6:7] nt
	s_add_u32 s6, s6, s8
	s_addc_u32 s7, s7, 0
	global_load_dword v45, v1, s[6:7] nt
	s_add_u32 s6, s6, s8
	s_addc_u32 s7, s7, 0
	global_load_dword v46, v1, s[6:7] nt
	s_add_u32 s6, s6, s8
	s_addc_u32 s7, s7, 0
	global_load_dword v47, v1, s[6:7] nt
	s_add_u32 s6, s6, s8
	s_addc_u32 s7, s7, 0
	global_load_dword v48, v1, s[6:7] nt
	s_add_u32 s6, s6, s8
	s_addc_u32 s7, s7, 0
	global_load_dword v49, v1, s[6:7] nt
	s_add_u32 s6, s6, s8
	s_addc_u32 s7, s7, 0
	global_load_dword v50, v1, s[6:7] nt
	s_add_u32 s6, s6, s8
	s_addc_u32 s7, s7, 0
	global_load_dword v51, v1, s[6:7] nt
	s_add_u32 s6, s6, s8
	s_addc_u32 s7, s7, 0
	global_load_dword v52, v1, s[6:7] nt
	s_add_u32 s6, s6, s8
	s_addc_u32 s7, s7, 0
	global_load_dword v53, v1, s[6:7] nt
	s_add_u32 s6, s6, s8
	s_addc_u32 s7, s7, 0
	global_load_dword v54, v1, s[6:7] nt
	s_add_u32 s6, s6, s8
	s_addc_u32 s7, s7, 0
	global_load_dword v55, v1, s[6:7] nt
	s_add_u32 s6, s6, s8
	s_addc_u32 s7, s7, 0
	global_load_dword v56, v1, s[6:7] nt
	s_add_u32 s6, s6, s8
	s_addc_u32 s7, s7, 0
	global_load_dword v57, v1, s[6:7] nt
	s_add_u32 s6, s6, s8
	s_addc_u32 s7, s7, 0
	global_load_dword v58, v1, s[6:7] nt
	s_add_u32 s6, s6, s8
	s_addc_u32 s7, s7, 0
	global_load_dword v59, v1, s[6:7] nt
	s_add_u32 s6, s6, s8
	s_addc_u32 s7, s7, 0
	global_load_dword v60, v1, s[6:7] nt
	s_add_u32 s6, s6, s8
	s_addc_u32 s7, s7, 0
	global_load_dword v61, v1, s[6:7] nt
	s_add_u32 s6, s6, s8
	s_addc_u32 s7, s7, 0
	global_load_dword v62, v1, s[6:7] nt
	s_add_u32 s6, s6, s8
	s_addc_u32 s7, s7, 0
	global_load_dword v63, v1, s[6:7] nt
	s_add_u32 s6, s6, s8
	s_addc_u32 s7, s7, 0
	global_load_dword v64, v1, s[6:7] nt
	s_add_u32 s6, s6, s8
	s_addc_u32 s7, s7, 0
	global_load_dword v65, v1, s[6:7] nt
	s_add_u32 s6, s6, s8
	s_addc_u32 s7, s7, 0
	global_load_dword v66, v1, s[6:7] nt
	s_add_u32 s6, s6, s8
	s_addc_u32 s7, s7, 0
	global_load_dword v67, v1, s[6:7] nt
	s_add_u32 s6, s6, s8
	s_addc_u32 s7, s7, 0
	global_load_dword v68, v1, s[6:7] nt
	s_add_u32 s6, s6, s8
	s_addc_u32 s7, s7, 0
	global_load_dword v69, v1, s[6:7] nt
	s_add_u32 s6, s6, s8
	s_addc_u32 s7, s7, 0
	global_load_dword v70, v1, s[6:7] nt
	s_add_u32 s6, s6, s8
	s_addc_u32 s7, s7, 0
	global_load_dword v71, v1, s[6:7] nt
	s_add_u32 s6, s6, s8
	s_addc_u32 s7, s7, 0
	global_load_dword v72, v1, s[6:7] nt
	s_add_u32 s6, s6, s8
	s_addc_u32 s7, s7, 0
	global_load_dword v73, v1, s[6:7] nt
	s_add_u32 s6, s6, s8
	s_addc_u32 s7, s7, 0
	global_load_dword v74, v1, s[6:7] nt
	s_add_u32 s6, s6, s8
	s_addc_u32 s7, s7, 0
	global_load_dword v75, v1, s[6:7] nt
	s_add_u32 s6, s6, s8
	s_addc_u32 s7, s7, 0
	global_load_dword v76, v1, s[6:7] nt
	s_add_u32 s6, s6, s8
	s_addc_u32 s7, s7, 0
	global_load_dword v77, v1, s[6:7] nt
	s_add_u32 s6, s6, s8
	s_addc_u32 s7, s7, 0
	global_load_dword v78, v1, s[6:7] nt
	s_add_u32 s6, s6, s8
	s_addc_u32 s7, s7, 0
	global_load_dword v79, v1, s[6:7] nt
	s_add_u32 s6, s6, s8
	s_addc_u32 s7, s7, 0
	s_waitcnt vmcnt(32)
	v_mul_f32_e32 v32, 0x42000000, v32
	v_mul_f32_e32 v33, 0x42000000, v33
	v_mul_f32_e32 v34, 0x42000000, v34
	v_mul_f32_e32 v35, 0x42000000, v35
	v_mul_f32_e32 v36, 0x42000000, v36
	v_mul_f32_e32 v37, 0x42000000, v37
	v_mul_f32_e32 v38, 0x42000000, v38
	v_mul_f32_e32 v39, 0x42000000, v39
	v_mul_f32_e32 v40, 0x42000000, v40
	v_mul_f32_e32 v41, 0x42000000, v41
	v_mul_f32_e32 v42, 0x42000000, v42
	v_mul_f32_e32 v43, 0x42000000, v43
	v_mul_f32_e32 v44, 0x42000000, v44
	v_mul_f32_e32 v45, 0x42000000, v45
	v_mul_f32_e32 v46, 0x42000000, v46
	v_mul_f32_e32 v47, 0x42000000, v47
	v_cvt_pk_fp8_f32 v4, v32, v33
	v_cvt_pk_fp8_f32 v5, v36, v37
	v_cvt_pk_fp8_f32 v6, v40, v41
	v_cvt_pk_fp8_f32 v7, v44, v45
	v_cvt_pk_fp8_f32 v4, v34, v35 op_sel:[0,0,1]
	v_cvt_pk_fp8_f32 v5, v38, v39 op_sel:[0,0,1]
	v_cvt_pk_fp8_f32 v6, v42, v43 op_sel:[0,0,1]
	v_cvt_pk_fp8_f32 v7, v46, v47 op_sel:[0,0,1]
	global_load_dword v80, v1, s[6:7] nt
	s_add_u32 s6, s6, s8
	s_addc_u32 s7, s7, 0
	global_load_dword v81, v1, s[6:7] nt
	s_add_u32 s6, s6, s8
	s_addc_u32 s7, s7, 0
	global_load_dword v82, v1, s[6:7] nt
	s_add_u32 s6, s6, s8
	s_addc_u32 s7, s7, 0
	global_load_dword v83, v1, s[6:7] nt
	s_add_u32 s6, s6, s8
	s_addc_u32 s7, s7, 0
	global_load_dword v84, v1, s[6:7] nt
	s_add_u32 s6, s6, s8
	s_addc_u32 s7, s7, 0
	global_load_dword v85, v1, s[6:7] nt
	s_add_u32 s6, s6, s8
	s_addc_u32 s7, s7, 0
	global_load_dword v86, v1, s[6:7] nt
	s_add_u32 s6, s6, s8
	s_addc_u32 s7, s7, 0
	global_load_dword v87, v1, s[6:7] nt
	s_add_u32 s6, s6, s8
	s_addc_u32 s7, s7, 0
	global_load_dword v88, v1, s[6:7] nt
	s_add_u32 s6, s6, s8
	s_addc_u32 s7, s7, 0
	global_load_dword v89, v1, s[6:7] nt
	s_add_u32 s6, s6, s8
	s_addc_u32 s7, s7, 0
	global_load_dword v90, v1, s[6:7] nt
	s_add_u32 s6, s6, s8
	s_addc_u32 s7, s7, 0
	global_load_dword v91, v1, s[6:7] nt
	s_add_u32 s6, s6, s8
	s_addc_u32 s7, s7, 0
	global_load_dword v92, v1, s[6:7] nt
	s_add_u32 s6, s6, s8
	s_addc_u32 s7, s7, 0
	global_load_dword v93, v1, s[6:7] nt
	s_add_u32 s6, s6, s8
	s_addc_u32 s7, s7, 0
	global_load_dword v94, v1, s[6:7] nt
	s_add_u32 s6, s6, s8
	s_addc_u32 s7, s7, 0
	global_load_dword v95, v1, s[6:7] nt
	s_add_u32 s6, s6, s8
	s_addc_u32 s7, s7, 0
	s_waitcnt vmcnt(32)
	v_mul_f32_e32 v48, 0x42000000, v48
	v_mul_f32_e32 v49, 0x42000000, v49
	v_mul_f32_e32 v50, 0x42000000, v50
	v_mul_f32_e32 v51, 0x42000000, v51
	v_mul_f32_e32 v52, 0x42000000, v52
	v_mul_f32_e32 v53, 0x42000000, v53
	v_mul_f32_e32 v54, 0x42000000, v54
	v_mul_f32_e32 v55, 0x42000000, v55
	v_mul_f32_e32 v56, 0x42000000, v56
	v_mul_f32_e32 v57, 0x42000000, v57
	v_mul_f32_e32 v58, 0x42000000, v58
	v_mul_f32_e32 v59, 0x42000000, v59
	v_mul_f32_e32 v60, 0x42000000, v60
	v_mul_f32_e32 v61, 0x42000000, v61
	v_mul_f32_e32 v62, 0x42000000, v62
	v_mul_f32_e32 v63, 0x42000000, v63
	v_cvt_pk_fp8_f32 v8, v48, v49
	v_cvt_pk_fp8_f32 v9, v52, v53
	v_cvt_pk_fp8_f32 v10, v56, v57
	v_cvt_pk_fp8_f32 v11, v60, v61
	v_cvt_pk_fp8_f32 v8, v50, v51 op_sel:[0,0,1]
	v_cvt_pk_fp8_f32 v9, v54, v55 op_sel:[0,0,1]
	v_cvt_pk_fp8_f32 v10, v58, v59 op_sel:[0,0,1]
	v_cvt_pk_fp8_f32 v11, v62, v63 op_sel:[0,0,1]
	s_waitcnt vmcnt(16)
	v_mul_f32_e32 v64, 0x42000000, v64
	v_mul_f32_e32 v65, 0x42000000, v65
	v_mul_f32_e32 v66, 0x42000000, v66
	v_mul_f32_e32 v67, 0x42000000, v67
	v_mul_f32_e32 v68, 0x42000000, v68
	v_mul_f32_e32 v69, 0x42000000, v69
	v_mul_f32_e32 v70, 0x42000000, v70
	v_mul_f32_e32 v71, 0x42000000, v71
	v_mul_f32_e32 v72, 0x42000000, v72
	v_mul_f32_e32 v73, 0x42000000, v73
	v_mul_f32_e32 v74, 0x42000000, v74
	v_mul_f32_e32 v75, 0x42000000, v75
	v_mul_f32_e32 v76, 0x42000000, v76
	v_mul_f32_e32 v77, 0x42000000, v77
	v_mul_f32_e32 v78, 0x42000000, v78
	v_mul_f32_e32 v79, 0x42000000, v79
	v_cvt_pk_fp8_f32 v12, v64, v65
	v_cvt_pk_fp8_f32 v13, v68, v69
	v_cvt_pk_fp8_f32 v14, v72, v73
	v_cvt_pk_fp8_f32 v15, v76, v77
	v_cvt_pk_fp8_f32 v12, v66, v67 op_sel:[0,0,1]
	v_cvt_pk_fp8_f32 v13, v70, v71 op_sel:[0,0,1]
	v_cvt_pk_fp8_f32 v14, v74, v75 op_sel:[0,0,1]
	v_cvt_pk_fp8_f32 v15, v78, v79 op_sel:[0,0,1]
	s_waitcnt vmcnt(0)
	v_mul_f32_e32 v80, 0x42000000, v80
	v_mul_f32_e32 v81, 0x42000000, v81
	v_mul_f32_e32 v82, 0x42000000, v82
	v_mul_f32_e32 v83, 0x42000000, v83
	v_mul_f32_e32 v84, 0x42000000, v84
	v_mul_f32_e32 v85, 0x42000000, v85
	v_mul_f32_e32 v86, 0x42000000, v86
	v_mul_f32_e32 v87, 0x42000000, v87
	v_mul_f32_e32 v88, 0x42000000, v88
	v_mul_f32_e32 v89, 0x42000000, v89
	v_mul_f32_e32 v90, 0x42000000, v90
	v_mul_f32_e32 v91, 0x42000000, v91
	v_mul_f32_e32 v92, 0x42000000, v92
	v_mul_f32_e32 v93, 0x42000000, v93
	v_mul_f32_e32 v94, 0x42000000, v94
	v_mul_f32_e32 v95, 0x42000000, v95
	v_cvt_pk_fp8_f32 v16, v80, v81
	v_cvt_pk_fp8_f32 v17, v84, v85
	v_cvt_pk_fp8_f32 v18, v88, v89
	v_cvt_pk_fp8_f32 v19, v92, v93
	v_cvt_pk_fp8_f32 v16, v82, v83 op_sel:[0,0,1]
	v_cvt_pk_fp8_f32 v17, v86, v87 op_sel:[0,0,1]
	v_cvt_pk_fp8_f32 v18, v90, v91 op_sel:[0,0,1]
	v_cvt_pk_fp8_f32 v19, v94, v95 op_sel:[0,0,1]
	s_mov_b64 vcc, s[42:43]
	s_nop 1
	v_cndmask_b32_dpp v24, v4, v8, vcc quad_perm:[1,0,3,2] row_mask:0xf bank_mask:0xf
	v_cndmask_b32_dpp v28, v12, v16, vcc quad_perm:[1,0,3,2] row_mask:0xf bank_mask:0xf
	v_cndmask_b32_dpp v25, v5, v9, vcc quad_perm:[1,0,3,2] row_mask:0xf bank_mask:0xf
	v_cndmask_b32_dpp v29, v13, v17, vcc quad_perm:[1,0,3,2] row_mask:0xf bank_mask:0xf
	v_cndmask_b32_dpp v26, v6, v10, vcc quad_perm:[1,0,3,2] row_mask:0xf bank_mask:0xf
	v_cndmask_b32_dpp v30, v14, v18, vcc quad_perm:[1,0,3,2] row_mask:0xf bank_mask:0xf
	v_cndmask_b32_dpp v27, v7, v11, vcc quad_perm:[1,0,3,2] row_mask:0xf bank_mask:0xf
	v_cndmask_b32_dpp v31, v15, v19, vcc quad_perm:[1,0,3,2] row_mask:0xf bank_mask:0xf
	s_mov_b64 vcc, s[44:45]
	s_nop 1
	v_cndmask_b32_dpp v4, v8, v4, vcc quad_perm:[1,0,3,2] row_mask:0xf bank_mask:0xf
	v_cndmask_b32_dpp v12, v16, v12, vcc quad_perm:[1,0,3,2] row_mask:0xf bank_mask:0xf
	v_cndmask_b32_dpp v5, v9, v5, vcc quad_perm:[1,0,3,2] row_mask:0xf bank_mask:0xf
	v_cndmask_b32_dpp v13, v17, v13, vcc quad_perm:[1,0,3,2] row_mask:0xf bank_mask:0xf
	v_cndmask_b32_dpp v6, v10, v6, vcc quad_perm:[1,0,3,2] row_mask:0xf bank_mask:0xf
	v_cndmask_b32_dpp v14, v18, v14, vcc quad_perm:[1,0,3,2] row_mask:0xf bank_mask:0xf
	v_cndmask_b32_dpp v7, v11, v7, vcc quad_perm:[1,0,3,2] row_mask:0xf bank_mask:0xf
	v_cndmask_b32_dpp v15, v19, v15, vcc quad_perm:[1,0,3,2] row_mask:0xf bank_mask:0xf
	s_mov_b64 vcc, s[46:47]
	s_nop 1
	v_cndmask_b32_dpp v8, v4, v12, vcc quad_perm:[2,3,0,1] row_mask:0xf bank_mask:0xf
	v_cndmask_b32_dpp v16, v24, v28, vcc quad_perm:[2,3,0,1] row_mask:0xf bank_mask:0xf
	v_cndmask_b32_dpp v9, v5, v13, vcc quad_perm:[2,3,0,1] row_mask:0xf bank_mask:0xf
	v_cndmask_b32_dpp v17, v25, v29, vcc quad_perm:[2,3,0,1] row_mask:0xf bank_mask:0xf
	v_cndmask_b32_dpp v10, v6, v14, vcc quad_perm:[2,3,0,1] row_mask:0xf bank_mask:0xf
	v_cndmask_b32_dpp v18, v26, v30, vcc quad_perm:[2,3,0,1] row_mask:0xf bank_mask:0xf
	v_cndmask_b32_dpp v11, v7, v15, vcc quad_perm:[2,3,0,1] row_mask:0xf bank_mask:0xf
	v_cndmask_b32_dpp v19, v27, v31, vcc quad_perm:[2,3,0,1] row_mask:0xf bank_mask:0xf
	s_mov_b64 vcc, s[48:49]
	s_nop 1
	v_cndmask_b32_dpp v4, v12, v4, vcc quad_perm:[2,3,0,1] row_mask:0xf bank_mask:0xf
	v_cndmask_b32_dpp v24, v28, v24, vcc quad_perm:[2,3,0,1] row_mask:0xf bank_mask:0xf
	v_cndmask_b32_dpp v5, v13, v5, vcc quad_perm:[2,3,0,1] row_mask:0xf bank_mask:0xf
	v_cndmask_b32_dpp v25, v29, v25, vcc quad_perm:[2,3,0,1] row_mask:0xf bank_mask:0xf
	v_cndmask_b32_dpp v6, v14, v6, vcc quad_perm:[2,3,0,1] row_mask:0xf bank_mask:0xf
	v_cndmask_b32_dpp v26, v30, v26, vcc quad_perm:[2,3,0,1] row_mask:0xf bank_mask:0xf
	v_cndmask_b32_dpp v7, v15, v7, vcc quad_perm:[2,3,0,1] row_mask:0xf bank_mask:0xf
	v_cndmask_b32_dpp v27, v31, v27, vcc quad_perm:[2,3,0,1] row_mask:0xf bank_mask:0xf
	global_store_dwordx4 v3, v[4:7], s[10:11] nt
	global_store_dwordx4 v21, v[24:27], s[10:11] nt
	global_store_dwordx4 v22, v[8:11], s[10:11] nt
	global_store_dwordx4 v23, v[16:19], s[10:11] nt
	s_add_i32 s3, s3, s26
	s_branch .Lp0w_loop
.Lp0w_plain:
	s_add_u32 s6, s36, s16
	s_addc_u32 s7, s37, 0
	s_add_u32 s10, s62, s17
	s_addc_u32 s11, s63, 0
	v_mad_u32_u24 v3, v100, s12, v101
	v_add_u32_e32 v21, s12, v3
	v_add_u32_e32 v22, s12, v21
	v_add_u32_e32 v23, s12, v22
	global_load_dword v32, v1, s[6:7] nt
	s_add_u32 s6, s6, s8
	s_addc_u32 s7, s7, 0
	global_load_dword v33, v1, s[6:7] nt
	s_add_u32 s6, s6, s8
	s_addc_u32 s7, s7, 0
	global_load_dword v34, v1, s[6:7] nt
	s_add_u32 s6, s6, s8
	s_addc_u32 s7, s7, 0
	global_load_dword v35, v1, s[6:7] nt
	s_add_u32 s6, s6, s8
	s_addc_u32 s7, s7, 0
	global_load_dword v36, v1, s[6:7] nt
	s_add_u32 s6, s6, s8
	s_addc_u32 s7, s7, 0
	global_load_dword v37, v1, s[6:7] nt
	s_add_u32 s6, s6, s8
	s_addc_u32 s7, s7, 0
	global_load_dword v38, v1, s[6:7] nt
	s_add_u32 s6, s6, s8
	s_addc_u32 s7, s7, 0
	global_load_dword v39, v1, s[6:7] nt
	s_add_u32 s6, s6, s8
	s_addc_u32 s7, s7, 0
	global_load_dword v40, v1, s[6:7] nt
	s_add_u32 s6, s6, s8
	s_addc_u32 s7, s7, 0
	global_load_dword v41, v1, s[6:7] nt
	s_add_u32 s6, s6, s8
	s_addc_u32 s7, s7, 0
	global_load_dword v42, v1, s[6:7] nt
	s_add_u32 s6, s6, s8
	s_addc_u32 s7, s7, 0
	global_load_dword v43, v1, s[6:7] nt
	s_add_u32 s6, s6, s8
	s_addc_u32 s7, s7, 0
	global_load_dword v44, v1, s[6:7] nt
	s_add_u32 s6, s6, s8
	s_addc_u32 s7, s7, 0
	global_load_dword v45, v1, s[6:7] nt
	s_add_u32 s6, s6, s8
	s_addc_u32 s7, s7, 0
	global_load_dword v46, v1, s[6:7] nt
	s_add_u32 s6, s6, s8
	s_addc_u32 s7, s7, 0
	global_load_dword v47, v1, s[6:7] nt
	s_add_u32 s6, s6, s8
	s_addc_u32 s7, s7, 0
	global_load_dword v48, v1, s[6:7] nt
	s_add_u32 s6, s6, s8
	s_addc_u32 s7, s7, 0
	global_load_dword v49, v1, s[6:7] nt
	s_add_u32 s6, s6, s8
	s_addc_u32 s7, s7, 0
	global_load_dword v50, v1, s[6:7] nt
	s_add_u32 s6, s6, s8
	s_addc_u32 s7, s7, 0
	global_load_dword v51, v1, s[6:7] nt
	s_add_u32 s6, s6, s8
	s_addc_u32 s7, s7, 0
	global_load_dword v52, v1, s[6:7] nt
	s_add_u32 s6, s6, s8
	s_addc_u32 s7, s7, 0
	global_load_dword v53, v1, s[6:7] nt
	s_add_u32 s6, s6, s8
	s_addc_u32 s7, s7, 0
	global_load_dword v54, v1, s[6:7] nt
	s_add_u32 s6, s6, s8
	s_addc_u32 s7, s7, 0
	global_load_dword v55, v1, s[6:7] nt
	s_add_u32 s6, s6, s8
	s_addc_u32 s7, s7, 0
	global_load_dword v56, v1, s[6:7] nt
	s_add_u32 s6, s6, s8
	s_addc_u32 s7, s7, 0
	global_load_dword v57, v1, s[6:7] nt
	s_add_u32 s6, s6, s8
	s_addc_u32 s7, s7, 0
	global_load_dword v58, v1, s[6:7] nt
	s_add_u32 s6, s6, s8
	s_addc_u32 s7, s7, 0
	global_load_dword v59, v1, s[6:7] nt
	s_add_u32 s6, s6, s8
	s_addc_u32 s7, s7, 0
	global_load_dword v60, v1, s[6:7] nt
	s_add_u32 s6, s6, s8
	s_addc_u32 s7, s7, 0
	global_load_dword v61, v1, s[6:7] nt
	s_add_u32 s6, s6, s8
	s_addc_u32 s7, s7, 0
	global_load_dword v62, v1, s[6:7] nt
	s_add_u32 s6, s6, s8
	s_addc_u32 s7, s7, 0
	global_load_dword v63, v1, s[6:7] nt
	s_add_u32 s6, s6, s8
	s_addc_u32 s7, s7, 0
	global_load_dword v64, v1, s[6:7] nt
	s_add_u32 s6, s6, s8
	s_addc_u32 s7, s7, 0
	global_load_dword v65, v1, s[6:7] nt
	s_add_u32 s6, s6, s8
	s_addc_u32 s7, s7, 0
	global_load_dword v66, v1, s[6:7] nt
	s_add_u32 s6, s6, s8
	s_addc_u32 s7, s7, 0
	global_load_dword v67, v1, s[6:7] nt
	s_add_u32 s6, s6, s8
	s_addc_u32 s7, s7, 0
	global_load_dword v68, v1, s[6:7] nt
	s_add_u32 s6, s6, s8
	s_addc_u32 s7, s7, 0
	global_load_dword v69, v1, s[6:7] nt
	s_add_u32 s6, s6, s8
	s_addc_u32 s7, s7, 0
	global_load_dword v70, v1, s[6:7] nt
	s_add_u32 s6, s6, s8
	s_addc_u32 s7, s7, 0
	global_load_dword v71, v1, s[6:7] nt
	s_add_u32 s6, s6, s8
	s_addc_u32 s7, s7, 0
	global_load_dword v72, v1, s[6:7] nt
	s_add_u32 s6, s6, s8
	s_addc_u32 s7, s7, 0
	global_load_dword v73, v1, s[6:7] nt
	s_add_u32 s6, s6, s8
	s_addc_u32 s7, s7, 0
	global_load_dword v74, v1, s[6:7] nt
	s_add_u32 s6, s6, s8
	s_addc_u32 s7, s7, 0
	global_load_dword v75, v1, s[6:7] nt
	s_add_u32 s6, s6, s8
	s_addc_u32 s7, s7, 0
	global_load_dword v76, v1, s[6:7] nt
	s_add_u32 s6, s6, s8
	s_addc_u32 s7, s7, 0
	global_load_dword v77, v1, s[6:7] nt
	s_add_u32 s6, s6, s8
	s_addc_u32 s7, s7, 0
	global_load_dword v78, v1, s[6:7] nt
	s_add_u32 s6, s6, s8
	s_addc_u32 s7, s7, 0
	global_load_dword v79, v1, s[6:7] nt
	s_add_u32 s6, s6, s8
	s_addc_u32 s7, s7, 0
	s_waitcnt vmcnt(32)
	v_mul_f32_e32 v32, 0x42000000, v32
	v_mul_f32_e32 v33, 0x42000000, v33
	v_mul_f32_e32 v34, 0x42000000, v34
	v_mul_f32_e32 v35, 0x42000000, v35
	v_mul_f32_e32 v36, 0x42000000, v36
	v_mul_f32_e32 v37, 0x42000000, v37
	v_mul_f32_e32 v38, 0x42000000, v38
	v_mul_f32_e32 v39, 0x42000000, v39
	v_mul_f32_e32 v40, 0x42000000, v40
	v_mul_f32_e32 v41, 0x42000000, v41
	v_mul_f32_e32 v42, 0x42000000, v42
	v_mul_f32_e32 v43, 0x42000000, v43
	v_mul_f32_e32 v44, 0x42000000, v44
	v_mul_f32_e32 v45, 0x42000000, v45
	v_mul_f32_e32 v46, 0x42000000, v46
	v_mul_f32_e32 v47, 0x42000000, v47
	v_cvt_pk_fp8_f32 v4, v32, v33
	v_cvt_pk_fp8_f32 v5, v36, v37
	v_cvt_pk_fp8_f32 v6, v40, v41
	v_cvt_pk_fp8_f32 v7, v44, v45
	v_cvt_pk_fp8_f32 v4, v34, v35 op_sel:[0,0,1]
	v_cvt_pk_fp8_f32 v5, v38, v39 op_sel:[0,0,1]
	v_cvt_pk_fp8_f32 v6, v42, v43 op_sel:[0,0,1]
	v_cvt_pk_fp8_f32 v7, v46, v47 op_sel:[0,0,1]
	global_load_dword v80, v1, s[6:7] nt
	s_add_u32 s6, s6, s8
	s_addc_u32 s7, s7, 0
	global_load_dword v81, v1, s[6:7] nt
	s_add_u32 s6, s6, s8
	s_addc_u32 s7, s7, 0
	global_load_dword v82, v1, s[6:7] nt
	s_add_u32 s6, s6, s8
	s_addc_u32 s7, s7, 0
	global_load_dword v83, v1, s[6:7] nt
	s_add_u32 s6, s6, s8
	s_addc_u32 s7, s7, 0
	global_load_dword v84, v1, s[6:7] nt
	s_add_u32 s6, s6, s8
	s_addc_u32 s7, s7, 0
	global_load_dword v85, v1, s[6:7] nt
	s_add_u32 s6, s6, s8
	s_addc_u32 s7, s7, 0
	global_load_dword v86, v1, s[6:7] nt
	s_add_u32 s6, s6, s8
	s_addc_u32 s7, s7, 0
	global_load_dword v87, v1, s[6:7] nt
	s_add_u32 s6, s6, s8
	s_addc_u32 s7, s7, 0
	global_load_dword v88, v1, s[6:7] nt
	s_add_u32 s6, s6, s8
	s_addc_u32 s7, s7, 0
	global_load_dword v89, v1, s[6:7] nt
	s_add_u32 s6, s6, s8
	s_addc_u32 s7, s7, 0
	global_load_dword v90, v1, s[6:7] nt
	s_add_u32 s6, s6, s8
	s_addc_u32 s7, s7, 0
	global_load_dword v91, v1, s[6:7] nt
	s_add_u32 s6, s6, s8
	s_addc_u32 s7, s7, 0
	global_load_dword v92, v1, s[6:7] nt
	s_add_u32 s6, s6, s8
	s_addc_u32 s7, s7, 0
	global_load_dword v93, v1, s[6:7] nt
	s_add_u32 s6, s6, s8
	s_addc_u32 s7, s7, 0
	global_load_dword v94, v1, s[6:7] nt
	s_add_u32 s6, s6, s8
	s_addc_u32 s7, s7, 0
	global_load_dword v95, v1, s[6:7] nt
	s_add_u32 s6, s6, s8
	s_addc_u32 s7, s7, 0
	s_waitcnt vmcnt(32)
	v_mul_f32_e32 v48, 0x42000000, v48
	v_mul_f32_e32 v49, 0x42000000, v49
	v_mul_f32_e32 v50, 0x42000000, v50
	v_mul_f32_e32 v51, 0x42000000, v51
	v_mul_f32_e32 v52, 0x42000000, v52
	v_mul_f32_e32 v53, 0x42000000, v53
	v_mul_f32_e32 v54, 0x42000000, v54
	v_mul_f32_e32 v55, 0x42000000, v55
	v_mul_f32_e32 v56, 0x42000000, v56
	v_mul_f32_e32 v57, 0x42000000, v57
	v_mul_f32_e32 v58, 0x42000000, v58
	v_mul_f32_e32 v59, 0x42000000, v59
	v_mul_f32_e32 v60, 0x42000000, v60
	v_mul_f32_e32 v61, 0x42000000, v61
	v_mul_f32_e32 v62, 0x42000000, v62
	v_mul_f32_e32 v63, 0x42000000, v63
	v_cvt_pk_fp8_f32 v8, v48, v49
	v_cvt_pk_fp8_f32 v9, v52, v53
	v_cvt_pk_fp8_f32 v10, v56, v57
	v_cvt_pk_fp8_f32 v11, v60, v61
	v_cvt_pk_fp8_f32 v8, v50, v51 op_sel:[0,0,1]
	v_cvt_pk_fp8_f32 v9, v54, v55 op_sel:[0,0,1]
	v_cvt_pk_fp8_f32 v10, v58, v59 op_sel:[0,0,1]
	v_cvt_pk_fp8_f32 v11, v62, v63 op_sel:[0,0,1]
	s_waitcnt vmcnt(16)
	v_mul_f32_e32 v64, 0x42000000, v64
	v_mul_f32_e32 v65, 0x42000000, v65
	v_mul_f32_e32 v66, 0x42000000, v66
	v_mul_f32_e32 v67, 0x42000000, v67
	v_mul_f32_e32 v68, 0x42000000, v68
	v_mul_f32_e32 v69, 0x42000000, v69
	v_mul_f32_e32 v70, 0x42000000, v70
	v_mul_f32_e32 v71, 0x42000000, v71
	v_mul_f32_e32 v72, 0x42000000, v72
	v_mul_f32_e32 v73, 0x42000000, v73
	v_mul_f32_e32 v74, 0x42000000, v74
	v_mul_f32_e32 v75, 0x42000000, v75
	v_mul_f32_e32 v76, 0x42000000, v76
	v_mul_f32_e32 v77, 0x42000000, v77
	v_mul_f32_e32 v78, 0x42000000, v78
	v_mul_f32_e32 v79, 0x42000000, v79
	v_cvt_pk_fp8_f32 v12, v64, v65
	v_cvt_pk_fp8_f32 v13, v68, v69
	v_cvt_pk_fp8_f32 v14, v72, v73
	v_cvt_pk_fp8_f32 v15, v76, v77
	v_cvt_pk_fp8_f32 v12, v66, v67 op_sel:[0,0,1]
	v_cvt_pk_fp8_f32 v13, v70, v71 op_sel:[0,0,1]
	v_cvt_pk_fp8_f32 v14, v74, v75 op_sel:[0,0,1]
	v_cvt_pk_fp8_f32 v15, v78, v79 op_sel:[0,0,1]
	s_waitcnt vmcnt(0)
	v_mul_f32_e32 v80, 0x42000000, v80
	v_mul_f32_e32 v81, 0x42000000, v81
	v_mul_f32_e32 v82, 0x42000000, v82
	v_mul_f32_e32 v83, 0x42000000, v83
	v_mul_f32_e32 v84, 0x42000000, v84
	v_mul_f32_e32 v85, 0x42000000, v85
	v_mul_f32_e32 v86, 0x42000000, v86
	v_mul_f32_e32 v87, 0x42000000, v87
	v_mul_f32_e32 v88, 0x42000000, v88
	v_mul_f32_e32 v89, 0x42000000, v89
	v_mul_f32_e32 v90, 0x42000000, v90
	v_mul_f32_e32 v91, 0x42000000, v91
	v_mul_f32_e32 v92, 0x42000000, v92
	v_mul_f32_e32 v93, 0x42000000, v93
	v_mul_f32_e32 v94, 0x42000000, v94
	v_mul_f32_e32 v95, 0x42000000, v95
	v_cvt_pk_fp8_f32 v16, v80, v81
	v_cvt_pk_fp8_f32 v17, v84, v85
	v_cvt_pk_fp8_f32 v18, v88, v89
	v_cvt_pk_fp8_f32 v19, v92, v93
	v_cvt_pk_fp8_f32 v16, v82, v83 op_sel:[0,0,1]
	v_cvt_pk_fp8_f32 v17, v86, v87 op_sel:[0,0,1]
	v_cvt_pk_fp8_f32 v18, v90, v91 op_sel:[0,0,1]
	v_cvt_pk_fp8_f32 v19, v94, v95 op_sel:[0,0,1]
	s_mov_b64 vcc, s[42:43]
	s_nop 1
	v_cndmask_b32_dpp v24, v4, v8, vcc quad_perm:[1,0,3,2] row_mask:0xf bank_mask:0xf
	v_cndmask_b32_dpp v28, v12, v16, vcc quad_perm:[1,0,3,2] row_mask:0xf bank_mask:0xf
	v_cndmask_b32_dpp v25, v5, v9, vcc quad_perm:[1,0,3,2] row_mask:0xf bank_mask:0xf
	v_cndmask_b32_dpp v29, v13, v17, vcc quad_perm:[1,0,3,2] row_mask:0xf bank_mask:0xf
	v_cndmask_b32_dpp v26, v6, v10, vcc quad_perm:[1,0,3,2] row_mask:0xf bank_mask:0xf
	v_cndmask_b32_dpp v30, v14, v18, vcc quad_perm:[1,0,3,2] row_mask:0xf bank_mask:0xf
	v_cndmask_b32_dpp v27, v7, v11, vcc quad_perm:[1,0,3,2] row_mask:0xf bank_mask:0xf
	v_cndmask_b32_dpp v31, v15, v19, vcc quad_perm:[1,0,3,2] row_mask:0xf bank_mask:0xf
	s_mov_b64 vcc, s[44:45]
	s_nop 1
	v_cndmask_b32_dpp v4, v8, v4, vcc quad_perm:[1,0,3,2] row_mask:0xf bank_mask:0xf
	v_cndmask_b32_dpp v12, v16, v12, vcc quad_perm:[1,0,3,2] row_mask:0xf bank_mask:0xf
	v_cndmask_b32_dpp v5, v9, v5, vcc quad_perm:[1,0,3,2] row_mask:0xf bank_mask:0xf
	v_cndmask_b32_dpp v13, v17, v13, vcc quad_perm:[1,0,3,2] row_mask:0xf bank_mask:0xf
	v_cndmask_b32_dpp v6, v10, v6, vcc quad_perm:[1,0,3,2] row_mask:0xf bank_mask:0xf
	v_cndmask_b32_dpp v14, v18, v14, vcc quad_perm:[1,0,3,2] row_mask:0xf bank_mask:0xf
	v_cndmask_b32_dpp v7, v11, v7, vcc quad_perm:[1,0,3,2] row_mask:0xf bank_mask:0xf
	v_cndmask_b32_dpp v15, v19, v15, vcc quad_perm:[1,0,3,2] row_mask:0xf bank_mask:0xf
	s_mov_b64 vcc, s[46:47]
	s_nop 1
	v_cndmask_b32_dpp v8, v4, v12, vcc quad_perm:[2,3,0,1] row_mask:0xf bank_mask:0xf
	v_cndmask_b32_dpp v16, v24, v28, vcc quad_perm:[2,3,0,1] row_mask:0xf bank_mask:0xf
	v_cndmask_b32_dpp v9, v5, v13, vcc quad_perm:[2,3,0,1] row_mask:0xf bank_mask:0xf
	v_cndmask_b32_dpp v17, v25, v29, vcc quad_perm:[2,3,0,1] row_mask:0xf bank_mask:0xf
	v_cndmask_b32_dpp v10, v6, v14, vcc quad_perm:[2,3,0,1] row_mask:0xf bank_mask:0xf
	v_cndmask_b32_dpp v18, v26, v30, vcc quad_perm:[2,3,0,1] row_mask:0xf bank_mask:0xf
	v_cndmask_b32_dpp v11, v7, v15, vcc quad_perm:[2,3,0,1] row_mask:0xf bank_mask:0xf
	v_cndmask_b32_dpp v19, v27, v31, vcc quad_perm:[2,3,0,1] row_mask:0xf bank_mask:0xf
	s_mov_b64 vcc, s[48:49]
	s_nop 1
	v_cndmask_b32_dpp v4, v12, v4, vcc quad_perm:[2,3,0,1] row_mask:0xf bank_mask:0xf
	v_cndmask_b32_dpp v24, v28, v24, vcc quad_perm:[2,3,0,1] row_mask:0xf bank_mask:0xf
	v_cndmask_b32_dpp v5, v13, v5, vcc quad_perm:[2,3,0,1] row_mask:0xf bank_mask:0xf
	v_cndmask_b32_dpp v25, v29, v25, vcc quad_perm:[2,3,0,1] row_mask:0xf bank_mask:0xf
	v_cndmask_b32_dpp v6, v14, v6, vcc quad_perm:[2,3,0,1] row_mask:0xf bank_mask:0xf
	v_cndmask_b32_dpp v26, v30, v26, vcc quad_perm:[2,3,0,1] row_mask:0xf bank_mask:0xf
	v_cndmask_b32_dpp v7, v15, v7, vcc quad_perm:[2,3,0,1] row_mask:0xf bank_mask:0xf
	v_cndmask_b32_dpp v27, v31, v27, vcc quad_perm:[2,3,0,1] row_mask:0xf bank_mask:0xf
	global_store_dwordx4 v3, v[4:7], s[10:11]
	global_store_dwordx4 v21, v[24:27], s[10:11]
	global_store_dwordx4 v22, v[8:11], s[10:11]
	global_store_dwordx4 v23, v[16:19], s[10:11]
	s_add_i32 s3, s3, s26
	s_branch .Lp0w_loop

.LBB0_218:
	s_cmp_lt_i32 s64, 3
	s_cselect_b64 s[0:1], -1, 0
	s_and_b64 s[22:23], s[0:1], s[4:5]
	s_andn2_b64 vcc, exec, s[22:23]
	s_mov_b32 s36, 1
	s_cbranch_vccnz .LBB0_351
	v_readlane_b32 s98, v239, 0
	s_lshr_b32 s98, s98, 6
	v_readlane_b32 s99, v239, 23
	s_add_i32 s98, s98, s99
	s_add_i32 s98, s98, 2048
	s_add_u32 s11, s60, 0xe000000
	s_addc_u32 s5, s61, 0
	s_add_u32 s6, s62, 0x2e000000
	s_addc_u32 s7, s63, 0
	s_add_u32 s0, s60, 0x8000000
	v_writelane_b32 v239, s0, 50
	s_addc_u32 s0, s61, 0
	v_writelane_b32 v239, s0, 52
	s_add_u32 s0, s62, 0x28000000
	v_writelane_b32 v239, s0, 54
	s_addc_u32 s0, s63, 0
	v_writelane_b32 v239, s0, 56
	s_add_u32 s0, s62, 0x30000000
	v_writelane_b32 v239, s0, 58
	s_addc_u32 s0, s63, 0
	s_add_u32 s8, s62, 0xe000000
	s_addc_u32 s9, s63, 0
	v_writelane_b32 v239, s0, 60
	s_add_u32 s0, s62, 0x36000000
	v_writelane_b32 v239, s0, 62
	s_addc_u32 s0, s63, 0
	v_writelane_b32 v238, s0, 0
	s_add_u32 s0, s62, 0x3c000000
	v_writelane_b32 v238, s0, 2
	s_addc_u32 s0, s63, 0
	v_writelane_b32 v238, s0, 4
	s_ashr_i32 s0, s96, 5
	s_ashr_i32 s1, s0, 31
	s_and_b32 s10, s96, 3
	s_lshl_b64 s[2:3], s[0:1], 21
	s_add_u32 s2, s60, s2
	s_addc_u32 s3, s61, s3
	s_lshl_b32 s4, s10, 8
	s_add_u32 s48, s2, s4
	s_addc_u32 s49, s3, 0
	s_lshl_b64 s[2:3], s[0:1], 19
	v_writelane_b32 v238, s11, 6
	s_add_u32 s1, s11, s2
	v_writelane_b32 v238, s5, 7
	s_addc_u32 s5, s5, s3
	s_lshl_b32 s34, s10, 6
	s_add_u32 s12, s1, s34
	s_addc_u32 s13, s5, 0
	s_add_u32 s1, s6, s2
	s_addc_u32 s2, s7, s3
	s_add_u32 s14, s1, s34
	s_addc_u32 s15, s2, 0
	s_mul_hi_i32 s1, s0, 0x280000
	s_mul_i32 s0, s0, 0x280000
	v_writelane_b32 v238, s6, 9
	s_add_u32 s0, s8, s0
	v_writelane_b32 v238, s7, 11
	s_addc_u32 s1, s9, s1
	v_writelane_b32 v238, s8, 13
	s_add_u32 s8, s0, s4
	v_writelane_b32 v238, s9, 15
	s_addc_u32 s9, s1, 0
	s_lshl_b32 s0, s10, 4
	s_add_u32 s44, s84, s0
	s_addc_u32 s45, s85, 0
	s_lshl_b32 s0, s96, 1
	s_and_b32 s3, s0, 56
	v_mov_b32_e32 v4, v0
	s_mov_b32 s20, 8
	s_mov_b32 s35, 0
	s_mov_b32 s55, 4
	s_movk_i32 s37, 0x400
	s_cmpk_lt_i32 s96, 0x400
	s_waitcnt vmcnt(0)
	v_readfirstlane_b32 s2, v4
	s_cbranch_scc1 .LBB0_222
	s_mov_b64 s[44:45], 0
	s_mov_b32 s5, 0
	s_cmpk_lt_u32 s96, 0x800
	s_mov_b32 s55, 1
	s_cbranch_scc1 .LBB0_223
	s_lshr_b32 s0, s96, 1
	s_and_b32 s4, s0, 14
	s_bfe_u32 s6, s96, 0x20002
	s_and_b32 s3, s0, 8
	s_cmpk_gt_u32 s96, 0xbff
	s_cselect_b64 s[0:1], -1, 0
	v_cndmask_b32_e64 v1, 0, 1, s[0:1]
	s_and_b64 s[0:1], s[0:1], exec
	s_cselect_b32 s0, 8, 4
	s_cselect_b32 s6, s4, s6
	s_movk_i32 s4, 0xf400
	s_cselect_b32 s36, 16, 4
	s_cselect_b32 s3, 0, s3
	s_cselect_b32 s20, 4, 8
	s_cselect_b32 s4, s4, 0xfffff800
	s_or_b32 s10, s10, s0
	s_mov_b32 s1, 0
	v_readfirstlane_b32 s35, v1
	s_lshl_b32 s0, s10, 6
	s_branch .LBB0_224

.LBB0_258:
	s_cmp_lg_u32 s35, 0
	s_cselect_b64 s[66:67], -1, 0
	s_min_i32 s0, s3, 4
	s_add_i32 s2, s0, s20
	s_cmp_eq_u32 s35, 0
	s_cselect_b64 s[86:87], -1, 0
	s_and_b64 s[0:1], s[86:87], exec
	s_cselect_b32 s0, s2, 8
	s_cmp_gt_u32 s98, 26623
	s_cselect_b32 s99, 0, 1
	s_cbranch_scc1 .Lp2w_x_skip
	v_mbcnt_lo_u32_b32 v178, -1, 0
	v_mbcnt_hi_u32_b32 v178, -1, v178
	v_and_b32_e32 v179, 60, v178
	v_lshlrev_b32_e32 v179, 10, v179
	v_and_b32_e32 v180, 3, v178
	v_lshl_or_b32 v179, v180, 4, v179
	v_add_u32_e32 v180, 0x400, v179
	v_add_u32_e32 v181, 0x800, v179
	v_add_u32_e32 v190, 0xc00, v179
	v_lshlrev_b32_e32 v178, 2, v178
	s_sub_i32 s23, s98, 2048
	s_cmp_lt_u32 s23, 16384
	s_cbranch_scc0 .Lp2w_dn_a
	s_lshr_b32 s29, s23, 9
	s_bfe_u32 s24, s23, 0x40005
	s_and_b32 s25, s23, 31
	s_lshl_b32 s30, s29, 23
	s_lshl_b32 s32, s24, 19
	s_add_i32 s30, s30, s32
	s_lshl_b32 s32, s25, 8
	s_add_i32 s30, s30, s32
	s_lshl_b32 s31, s29, 11
	s_bfe_u32 s32, s25, 0x30001
	s_lshl_b32 s32, s32, 8
	s_add_i32 s31, s31, s32
	s_lshr_b32 s32, s25, 4
	s_lshl_b32 s32, s32, 7
	s_add_i32 s31, s31, s32
	s_and_b32 s32, s25, 1
	s_lshl_b32 s32, s32, 6
	s_add_i32 s31, s31, s32
	s_lshl_b32 s31, s31, 10
	s_lshl_b32 s32, s24, 6
	s_add_i32 s31, s31, s32
	s_add_i32 s31, s31, 0x2000000
	v_readlane_b32 s82, v239, 11
	v_readlane_b32 s83, v239, 12
	s_movk_i32 s97, 8192
	s_branch .Lp2w_go_a
.Lp2w_dn_a:
	s_sub_i32 s23, s23, 16384
	s_lshr_b32 s29, s23, 8
	s_bfe_u32 s24, s23, 0x40004
	s_and_b32 s25, s23, 15
	s_lshl_b32 s30, s29, 22
	s_lshl_b32 s32, s24, 18
	s_add_i32 s30, s30, s32
	s_lshl_b32 s32, s25, 8
	s_add_i32 s30, s30, s32
	s_lshl_b32 s31, s29, 20
	s_lshl_b32 s32, s25, 16
	s_add_i32 s31, s31, s32
	s_lshl_b32 s32, s24, 6
	s_add_i32 s31, s31, s32
	s_add_i32 s31, s31, 0x6000000
	v_readlane_b32 s82, v239, 15
	v_readlane_b32 s83, v239, 16
	s_movk_i32 s97, 4096
.Lp2w_go_a:
	v_readlane_b32 s62, v239, 44
	v_readlane_b32 s63, v239, 45
	s_add_u32 s100, s82, s30
	s_addc_u32 s101, s83, 0
	s_add_u32 s70, s62, s31
	s_addc_u32 s71, s63, 0
	global_load_dword v34, v178, s[100:101] nt
	s_add_u32 s100, s100, s97
	s_addc_u32 s101, s101, 0
	global_load_dword v35, v178, s[100:101] nt
	s_add_u32 s100, s100, s97
	s_addc_u32 s101, s101, 0
	global_load_dword v36, v178, s[100:101] nt
	s_add_u32 s100, s100, s97
	s_addc_u32 s101, s101, 0
	global_load_dword v37, v178, s[100:101] nt
	s_add_u32 s100, s100, s97
	s_addc_u32 s101, s101, 0
	global_load_dword v38, v178, s[100:101] nt
	s_add_u32 s100, s100, s97
	s_addc_u32 s101, s101, 0
	global_load_dword v39, v178, s[100:101] nt
	s_add_u32 s100, s100, s97
	s_addc_u32 s101, s101, 0
	global_load_dword v40, v178, s[100:101] nt
	s_add_u32 s100, s100, s97
	s_addc_u32 s101, s101, 0
	global_load_dword v41, v178, s[100:101] nt
	s_add_u32 s100, s100, s97
	s_addc_u32 s101, s101, 0
	global_load_dword v42, v178, s[100:101] nt
	s_add_u32 s100, s100, s97
	s_addc_u32 s101, s101, 0
	global_load_dword v43, v178, s[100:101] nt
	s_add_u32 s100, s100, s97
	s_addc_u32 s101, s101, 0
	global_load_dword v44, v178, s[100:101] nt
	s_add_u32 s100, s100, s97
	s_addc_u32 s101, s101, 0
	global_load_dword v45, v178, s[100:101] nt
	s_add_u32 s100, s100, s97
	s_addc_u32 s101, s101, 0
	global_load_dword v46, v178, s[100:101] nt
	s_add_u32 s100, s100, s97
	s_addc_u32 s101, s101, 0
	global_load_dword v47, v178, s[100:101] nt
	s_add_u32 s100, s100, s97
	s_addc_u32 s101, s101, 0
	global_load_dword v48, v178, s[100:101] nt
	s_add_u32 s100, s100, s97
	s_addc_u32 s101, s101, 0
	global_load_dword v49, v178, s[100:101] nt
	s_add_u32 s100, s100, s97
	s_addc_u32 s101, s101, 0
	global_load_dword v50, v178, s[100:101] nt
	s_add_u32 s100, s100, s97
	s_addc_u32 s101, s101, 0
	global_load_dword v51, v178, s[100:101] nt
	s_add_u32 s100, s100, s97
	s_addc_u32 s101, s101, 0
	global_load_dword v52, v178, s[100:101] nt
	s_add_u32 s100, s100, s97
	s_addc_u32 s101, s101, 0
	global_load_dword v53, v178, s[100:101] nt
	s_add_u32 s100, s100, s97
	s_addc_u32 s101, s101, 0
	global_load_dword v54, v178, s[100:101] nt
	s_add_u32 s100, s100, s97
	s_addc_u32 s101, s101, 0
	global_load_dword v55, v178, s[100:101] nt
	s_add_u32 s100, s100, s97
	s_addc_u32 s101, s101, 0
	global_load_dword v56, v178, s[100:101] nt
	s_add_u32 s100, s100, s97
	s_addc_u32 s101, s101, 0
	global_load_dword v57, v178, s[100:101] nt
	s_add_u32 s100, s100, s97
	s_addc_u32 s101, s101, 0
	global_load_dword v58, v178, s[100:101] nt
	s_add_u32 s100, s100, s97
	s_addc_u32 s101, s101, 0
	global_load_dword v59, v178, s[100:101] nt
	s_add_u32 s100, s100, s97
	s_addc_u32 s101, s101, 0
	global_load_dword v60, v178, s[100:101] nt
	s_add_u32 s100, s100, s97
	s_addc_u32 s101, s101, 0
	global_load_dword v61, v178, s[100:101] nt
	s_add_u32 s100, s100, s97
	s_addc_u32 s101, s101, 0
	global_load_dword v62, v178, s[100:101] nt
	s_add_u32 s100, s100, s97
	s_addc_u32 s101, s101, 0
	global_load_dword v63, v178, s[100:101] nt
	s_add_u32 s100, s100, s97
	s_addc_u32 s101, s101, 0
	global_load_dword v64, v178, s[100:101] nt
	s_add_u32 s100, s100, s97
	s_addc_u32 s101, s101, 0
	global_load_dword v65, v178, s[100:101] nt
	s_add_u32 s100, s100, s97
	s_addc_u32 s101, s101, 0
	global_load_dword v66, v178, s[100:101] nt
	s_add_u32 s100, s100, s97
	s_addc_u32 s101, s101, 0
	global_load_dword v67, v178, s[100:101] nt
	s_add_u32 s100, s100, s97
	s_addc_u32 s101, s101, 0
	global_load_dword v68, v178, s[100:101] nt
	s_add_u32 s100, s100, s97
	s_addc_u32 s101, s101, 0
	global_load_dword v69, v178, s[100:101] nt
	s_add_u32 s100, s100, s97
	s_addc_u32 s101, s101, 0
	global_load_dword v70, v178, s[100:101] nt
	s_add_u32 s100, s100, s97
	s_addc_u32 s101, s101, 0
	global_load_dword v71, v178, s[100:101] nt
	s_add_u32 s100, s100, s97
	s_addc_u32 s101, s101, 0
	global_load_dword v72, v178, s[100:101] nt
	s_add_u32 s100, s100, s97
	s_addc_u32 s101, s101, 0
	global_load_dword v73, v178, s[100:101] nt
	s_add_u32 s100, s100, s97
	s_addc_u32 s101, s101, 0
	global_load_dword v74, v178, s[100:101] nt
	s_add_u32 s100, s100, s97
	s_addc_u32 s101, s101, 0
	global_load_dword v75, v178, s[100:101] nt
	s_add_u32 s100, s100, s97
	s_addc_u32 s101, s101, 0
	global_load_dword v76, v178, s[100:101] nt
	s_add_u32 s100, s100, s97
	s_addc_u32 s101, s101, 0
	global_load_dword v77, v178, s[100:101] nt
	s_add_u32 s100, s100, s97
	s_addc_u32 s101, s101, 0
	global_load_dword v78, v178, s[100:101] nt
	s_add_u32 s100, s100, s97
	s_addc_u32 s101, s101, 0
	global_load_dword v79, v178, s[100:101] nt
	s_add_u32 s100, s100, s97
	s_addc_u32 s101, s101, 0
	global_load_dword v80, v178, s[100:101] nt
	s_add_u32 s100, s100, s97
	s_addc_u32 s101, s101, 0
	global_load_dword v81, v178, s[100:101] nt
	s_add_u32 s100, s100, s97
	s_addc_u32 s101, s101, 0
	s_waitcnt vmcnt(48)
	s_branch .Lp2w_x_done

.Lp2w_x_done:
	v_cvt_scalef32_pk_bf16_fp8 v4, v114, 1.0
	v_cvt_scalef32_pk_bf16_fp8 v5, v114, 1.0 op_sel:[1,0,0]
	v_cvt_scalef32_pk_bf16_fp8 v6, v115, 1.0
	v_cvt_scalef32_pk_bf16_fp8 v7, v115, 1.0 op_sel:[1,0,0]
	v_cvt_scalef32_pk_bf16_fp8 v8, v116, 1.0
	v_cvt_scalef32_pk_bf16_fp8 v9, v116, 1.0 op_sel:[1,0,0]
	v_cvt_scalef32_pk_bf16_fp8 v10, v117, 1.0
	v_cvt_scalef32_pk_bf16_fp8 v11, v117, 1.0 op_sel:[1,0,0]
	ds_write_b128 v196, v[4:7]
	ds_write_b128 v196, v[8:11] offset:16
	v_cvt_scalef32_pk_bf16_fp8 v4, v118, 1.0
	v_cvt_scalef32_pk_bf16_fp8 v5, v118, 1.0 op_sel:[1,0,0]
	v_cvt_scalef32_pk_bf16_fp8 v6, v119, 1.0
	v_cvt_scalef32_pk_bf16_fp8 v7, v119, 1.0 op_sel:[1,0,0]
	v_cvt_scalef32_pk_bf16_fp8 v8, v120, 1.0
	v_cvt_scalef32_pk_bf16_fp8 v9, v120, 1.0 op_sel:[1,0,0]
	v_cvt_scalef32_pk_bf16_fp8 v10, v121, 1.0
	v_cvt_scalef32_pk_bf16_fp8 v11, v121, 1.0 op_sel:[1,0,0]
	s_cmp_lt_i32 s0, 5
	ds_write_b128 v197, v[4:7]
	ds_write_b128 v197, v[8:11] offset:16
	s_cbranch_scc1 .LBB0_262
	v_cvt_scalef32_pk_bf16_fp8 v4, v122, 1.0
	v_cvt_scalef32_pk_bf16_fp8 v5, v122, 1.0 op_sel:[1,0,0]
	v_cvt_scalef32_pk_bf16_fp8 v6, v123, 1.0
	v_cvt_scalef32_pk_bf16_fp8 v7, v123, 1.0 op_sel:[1,0,0]
	v_cvt_scalef32_pk_bf16_fp8 v8, v124, 1.0
	v_cvt_scalef32_pk_bf16_fp8 v9, v124, 1.0 op_sel:[1,0,0]
	v_cvt_scalef32_pk_bf16_fp8 v10, v125, 1.0
	v_cvt_scalef32_pk_bf16_fp8 v11, v125, 1.0 op_sel:[1,0,0]
	ds_write_b128 v198, v[4:7]
	ds_write_b128 v198, v[8:11] offset:16
	s_cmp_lt_i32 s0, 7
	s_cbranch_scc0 .LBB0_263

.LBB0_266:
	s_add_i32 s60, s60, s74
	s_cmpk_lt_i32 s60, 0x1000
	s_waitcnt lgkmcnt(0)
	s_barrier
	s_cselect_b64 s[90:91], -1, 0
	s_cmpk_gt_i32 s60, 0xfff
	s_cselect_b64 s[64:65], -1, 0
	s_cmp_eq_u32 s99, 0
	s_cbranch_scc1 .Lp2w_y_skip
	s_waitcnt vmcnt(32)
	v_mul_f32_e32 v34, 0x42000000, v34
	v_mul_f32_e32 v35, 0x42000000, v35
	v_mul_f32_e32 v36, 0x42000000, v36
	v_mul_f32_e32 v37, 0x42000000, v37
	v_mul_f32_e32 v38, 0x42000000, v38
	v_mul_f32_e32 v39, 0x42000000, v39
	v_mul_f32_e32 v40, 0x42000000, v40
	v_mul_f32_e32 v41, 0x42000000, v41
	v_mul_f32_e32 v42, 0x42000000, v42
	v_mul_f32_e32 v43, 0x42000000, v43
	v_mul_f32_e32 v44, 0x42000000, v44
	v_mul_f32_e32 v45, 0x42000000, v45
	v_mul_f32_e32 v46, 0x42000000, v46
	v_mul_f32_e32 v47, 0x42000000, v47
	v_mul_f32_e32 v48, 0x42000000, v48
	v_mul_f32_e32 v49, 0x42000000, v49
	v_cvt_pk_fp8_f32 v154, v34, v35
	v_cvt_pk_fp8_f32 v155, v38, v39
	v_cvt_pk_fp8_f32 v156, v42, v43
	v_cvt_pk_fp8_f32 v157, v46, v47
	v_cvt_pk_fp8_f32 v154, v36, v37 op_sel:[0,0,1]
	v_cvt_pk_fp8_f32 v155, v40, v41 op_sel:[0,0,1]
	v_cvt_pk_fp8_f32 v156, v44, v45 op_sel:[0,0,1]
	v_cvt_pk_fp8_f32 v157, v48, v49 op_sel:[0,0,1]
	global_load_dword v82, v178, s[100:101] nt
	s_add_u32 s100, s100, s97
	s_addc_u32 s101, s101, 0
	global_load_dword v83, v178, s[100:101] nt
	s_add_u32 s100, s100, s97
	s_addc_u32 s101, s101, 0
	global_load_dword v84, v178, s[100:101] nt
	s_add_u32 s100, s100, s97
	s_addc_u32 s101, s101, 0
	global_load_dword v85, v178, s[100:101] nt
	s_add_u32 s100, s100, s97
	s_addc_u32 s101, s101, 0
	global_load_dword v86, v178, s[100:101] nt
	s_add_u32 s100, s100, s97
	s_addc_u32 s101, s101, 0
	global_load_dword v87, v178, s[100:101] nt
	s_add_u32 s100, s100, s97
	s_addc_u32 s101, s101, 0
	global_load_dword v88, v178, s[100:101] nt
	s_add_u32 s100, s100, s97
	s_addc_u32 s101, s101, 0
	global_load_dword v89, v178, s[100:101] nt
	s_add_u32 s100, s100, s97
	s_addc_u32 s101, s101, 0
	global_load_dword v90, v178, s[100:101] nt
	s_add_u32 s100, s100, s97
	s_addc_u32 s101, s101, 0
	global_load_dword v91, v178, s[100:101] nt
	s_add_u32 s100, s100, s97
	s_addc_u32 s101, s101, 0
	global_load_dword v92, v178, s[100:101] nt
	s_add_u32 s100, s100, s97
	s_addc_u32 s101, s101, 0
	global_load_dword v93, v178, s[100:101] nt
	s_add_u32 s100, s100, s97
	s_addc_u32 s101, s101, 0
	global_load_dword v94, v178, s[100:101] nt
	s_add_u32 s100, s100, s97
	s_addc_u32 s101, s101, 0
	global_load_dword v95, v178, s[100:101] nt
	s_add_u32 s100, s100, s97
	s_addc_u32 s101, s101, 0
	global_load_dword v96, v178, s[100:101] nt
	s_add_u32 s100, s100, s97
	s_addc_u32 s101, s101, 0
	global_load_dword v97, v178, s[100:101] nt
	s_add_u32 s100, s100, s97
	s_addc_u32 s101, s101, 0
	s_waitcnt vmcnt(32)
	v_mul_f32_e32 v50, 0x42000000, v50
	v_mul_f32_e32 v51, 0x42000000, v51
	v_mul_f32_e32 v52, 0x42000000, v52
	v_mul_f32_e32 v53, 0x42000000, v53
	v_mul_f32_e32 v54, 0x42000000, v54
	v_mul_f32_e32 v55, 0x42000000, v55
	v_mul_f32_e32 v56, 0x42000000, v56
	v_mul_f32_e32 v57, 0x42000000, v57
	v_mul_f32_e32 v58, 0x42000000, v58
	v_mul_f32_e32 v59, 0x42000000, v59
	v_mul_f32_e32 v60, 0x42000000, v60
	v_mul_f32_e32 v61, 0x42000000, v61
	v_mul_f32_e32 v62, 0x42000000, v62
	v_mul_f32_e32 v63, 0x42000000, v63
	v_mul_f32_e32 v64, 0x42000000, v64
	v_mul_f32_e32 v65, 0x42000000, v65
	v_cvt_pk_fp8_f32 v158, v50, v51
	v_cvt_pk_fp8_f32 v159, v54, v55
	v_cvt_pk_fp8_f32 v160, v58, v59
	v_cvt_pk_fp8_f32 v161, v62, v63
	v_cvt_pk_fp8_f32 v158, v52, v53 op_sel:[0,0,1]
	v_cvt_pk_fp8_f32 v159, v56, v57 op_sel:[0,0,1]
	v_cvt_pk_fp8_f32 v160, v60, v61 op_sel:[0,0,1]
	v_cvt_pk_fp8_f32 v161, v64, v65 op_sel:[0,0,1]
	s_waitcnt vmcnt(16)
	v_mul_f32_e32 v66, 0x42000000, v66
	v_mul_f32_e32 v67, 0x42000000, v67
	v_mul_f32_e32 v68, 0x42000000, v68
	v_mul_f32_e32 v69, 0x42000000, v69
	v_mul_f32_e32 v70, 0x42000000, v70
	v_mul_f32_e32 v71, 0x42000000, v71
	v_mul_f32_e32 v72, 0x42000000, v72
	v_mul_f32_e32 v73, 0x42000000, v73
	v_mul_f32_e32 v74, 0x42000000, v74
	v_mul_f32_e32 v75, 0x42000000, v75
	v_mul_f32_e32 v76, 0x42000000, v76
	v_mul_f32_e32 v77, 0x42000000, v77
	v_mul_f32_e32 v78, 0x42000000, v78
	v_mul_f32_e32 v79, 0x42000000, v79
	v_mul_f32_e32 v80, 0x42000000, v80
	v_mul_f32_e32 v81, 0x42000000, v81
	v_cvt_pk_fp8_f32 v162, v66, v67
	v_cvt_pk_fp8_f32 v163, v70, v71
	v_cvt_pk_fp8_f32 v164, v74, v75
	v_cvt_pk_fp8_f32 v165, v78, v79
	v_cvt_pk_fp8_f32 v162, v68, v69 op_sel:[0,0,1]
	v_cvt_pk_fp8_f32 v163, v72, v73 op_sel:[0,0,1]
	v_cvt_pk_fp8_f32 v164, v76, v77 op_sel:[0,0,1]
	v_cvt_pk_fp8_f32 v165, v80, v81 op_sel:[0,0,1]
	s_waitcnt vmcnt(0)
	v_mul_f32_e32 v82, 0x42000000, v82
	v_mul_f32_e32 v83, 0x42000000, v83
	v_mul_f32_e32 v84, 0x42000000, v84
	v_mul_f32_e32 v85, 0x42000000, v85
	v_mul_f32_e32 v86, 0x42000000, v86
	v_mul_f32_e32 v87, 0x42000000, v87
	v_mul_f32_e32 v88, 0x42000000, v88
	v_mul_f32_e32 v89, 0x42000000, v89
	v_mul_f32_e32 v90, 0x42000000, v90
	v_mul_f32_e32 v91, 0x42000000, v91
	v_mul_f32_e32 v92, 0x42000000, v92
	v_mul_f32_e32 v93, 0x42000000, v93
	v_mul_f32_e32 v94, 0x42000000, v94
	v_mul_f32_e32 v95, 0x42000000, v95
	v_mul_f32_e32 v96, 0x42000000, v96
	v_mul_f32_e32 v97, 0x42000000, v97
	v_cvt_pk_fp8_f32 v166, v82, v83
	v_cvt_pk_fp8_f32 v167, v86, v87
	v_cvt_pk_fp8_f32 v168, v90, v91
	v_cvt_pk_fp8_f32 v169, v94, v95
	v_cvt_pk_fp8_f32 v166, v84, v85 op_sel:[0,0,1]
	v_cvt_pk_fp8_f32 v167, v88, v89 op_sel:[0,0,1]
	v_cvt_pk_fp8_f32 v168, v92, v93 op_sel:[0,0,1]
	v_cvt_pk_fp8_f32 v169, v96, v97 op_sel:[0,0,1]
	s_mov_b32 vcc_lo, 0xaaaaaaaa
	s_mov_b32 vcc_hi, 0xaaaaaaaa
	s_nop 1
	v_cndmask_b32_dpp v170, v154, v158, vcc quad_perm:[1,0,3,2] row_mask:0xf bank_mask:0xf
	v_cndmask_b32_dpp v174, v162, v166, vcc quad_perm:[1,0,3,2] row_mask:0xf bank_mask:0xf
	v_cndmask_b32_dpp v171, v155, v159, vcc quad_perm:[1,0,3,2] row_mask:0xf bank_mask:0xf
	v_cndmask_b32_dpp v175, v163, v167, vcc quad_perm:[1,0,3,2] row_mask:0xf bank_mask:0xf
	v_cndmask_b32_dpp v172, v156, v160, vcc quad_perm:[1,0,3,2] row_mask:0xf bank_mask:0xf
	v_cndmask_b32_dpp v176, v164, v168, vcc quad_perm:[1,0,3,2] row_mask:0xf bank_mask:0xf
	v_cndmask_b32_dpp v173, v157, v161, vcc quad_perm:[1,0,3,2] row_mask:0xf bank_mask:0xf
	v_cndmask_b32_dpp v177, v165, v169, vcc quad_perm:[1,0,3,2] row_mask:0xf bank_mask:0xf
	s_mov_b32 vcc_lo, 0x55555555
	s_mov_b32 vcc_hi, 0x55555555
	s_nop 1
	v_cndmask_b32_dpp v154, v158, v154, vcc quad_perm:[1,0,3,2] row_mask:0xf bank_mask:0xf
	v_cndmask_b32_dpp v162, v166, v162, vcc quad_perm:[1,0,3,2] row_mask:0xf bank_mask:0xf
	v_cndmask_b32_dpp v155, v159, v155, vcc quad_perm:[1,0,3,2] row_mask:0xf bank_mask:0xf
	v_cndmask_b32_dpp v163, v167, v163, vcc quad_perm:[1,0,3,2] row_mask:0xf bank_mask:0xf
	v_cndmask_b32_dpp v156, v160, v156, vcc quad_perm:[1,0,3,2] row_mask:0xf bank_mask:0xf
	v_cndmask_b32_dpp v164, v168, v164, vcc quad_perm:[1,0,3,2] row_mask:0xf bank_mask:0xf
	v_cndmask_b32_dpp v157, v161, v157, vcc quad_perm:[1,0,3,2] row_mask:0xf bank_mask:0xf
	v_cndmask_b32_dpp v165, v169, v165, vcc quad_perm:[1,0,3,2] row_mask:0xf bank_mask:0xf
	s_mov_b32 vcc_lo, 0xcccccccc
	s_mov_b32 vcc_hi, 0xcccccccc
	s_nop 1
	v_cndmask_b32_dpp v158, v154, v162, vcc quad_perm:[2,3,0,1] row_mask:0xf bank_mask:0xf
	v_cndmask_b32_dpp v166, v170, v174, vcc quad_perm:[2,3,0,1] row_mask:0xf bank_mask:0xf
	v_cndmask_b32_dpp v159, v155, v163, vcc quad_perm:[2,3,0,1] row_mask:0xf bank_mask:0xf
	v_cndmask_b32_dpp v167, v171, v175, vcc quad_perm:[2,3,0,1] row_mask:0xf bank_mask:0xf
	v_cndmask_b32_dpp v160, v156, v164, vcc quad_perm:[2,3,0,1] row_mask:0xf bank_mask:0xf
	v_cndmask_b32_dpp v168, v172, v176, vcc quad_perm:[2,3,0,1] row_mask:0xf bank_mask:0xf
	v_cndmask_b32_dpp v161, v157, v165, vcc quad_perm:[2,3,0,1] row_mask:0xf bank_mask:0xf
	v_cndmask_b32_dpp v169, v173, v177, vcc quad_perm:[2,3,0,1] row_mask:0xf bank_mask:0xf
	s_mov_b32 vcc_lo, 0x33333333
	s_mov_b32 vcc_hi, 0x33333333
	s_nop 1
	v_cndmask_b32_dpp v154, v162, v154, vcc quad_perm:[2,3,0,1] row_mask:0xf bank_mask:0xf
	v_cndmask_b32_dpp v170, v174, v170, vcc quad_perm:[2,3,0,1] row_mask:0xf bank_mask:0xf
	v_cndmask_b32_dpp v155, v163, v155, vcc quad_perm:[2,3,0,1] row_mask:0xf bank_mask:0xf
	v_cndmask_b32_dpp v171, v175, v171, vcc quad_perm:[2,3,0,1] row_mask:0xf bank_mask:0xf
	v_cndmask_b32_dpp v156, v164, v156, vcc quad_perm:[2,3,0,1] row_mask:0xf bank_mask:0xf
	v_cndmask_b32_dpp v172, v176, v172, vcc quad_perm:[2,3,0,1] row_mask:0xf bank_mask:0xf
	v_cndmask_b32_dpp v157, v165, v157, vcc quad_perm:[2,3,0,1] row_mask:0xf bank_mask:0xf
	v_cndmask_b32_dpp v173, v177, v173, vcc quad_perm:[2,3,0,1] row_mask:0xf bank_mask:0xf
	global_store_dwordx4 v179, v[154:157], s[70:71] nt
	global_store_dwordx4 v180, v[170:173], s[70:71] nt
	global_store_dwordx4 v181, v[158:161], s[70:71] nt
	global_store_dwordx4 v190, v[166:169], s[70:71] nt
	s_lshl_b32 s23, s74, 3
	s_add_i32 s98, s98, s23
.Lp2w_y_skip:
	s_and_b64 vcc, exec, s[64:65]
	s_cbranch_vccnz .LBB0_278
	s_cmpk_gt_i32 s60, 0x3ff
	s_mov_b64 s[10:11], -1
	s_cbranch_scc0 .LBB0_276
	s_and_b32 s4, s60, 3
	s_cmpk_gt_u32 s60, 0x7ff
	s_mov_b64 s[0:1], -1
	s_cbranch_scc0 .LBB0_273
	s_cmpk_gt_u32 s60, 0xbff
	s_cbranch_scc0 .LBB0_271
	s_lshr_b32 s0, s60, 1
	s_add_i32 s2, s60, 0xfffff400
	s_or_b32 s10, s4, 8
	s_and_b32 s5, s0, 14
	s_mov_b64 s[0:1], 0

.LBB0_350:
.Lp2w_tail:
	s_cmp_gt_u32 s98, 26623
	s_cbranch_scc1 .Lp2w_tail_done
	v_mbcnt_lo_u32_b32 v178, -1, 0
	v_mbcnt_hi_u32_b32 v178, -1, v178
	v_and_b32_e32 v179, 60, v178
	v_lshlrev_b32_e32 v179, 10, v179
	v_and_b32_e32 v180, 3, v178
	v_lshl_or_b32 v179, v180, 4, v179
	v_add_u32_e32 v180, 0x400, v179
	v_add_u32_e32 v181, 0x800, v179
	v_add_u32_e32 v190, 0xc00, v179
	v_lshlrev_b32_e32 v178, 2, v178
	s_sub_i32 s23, s98, 2048
	s_cmp_lt_u32 s23, 16384
	s_cbranch_scc0 .Lp2w_dn_b
	s_lshr_b32 s29, s23, 9
	s_bfe_u32 s24, s23, 0x40005
	s_and_b32 s25, s23, 31
	s_lshl_b32 s30, s29, 23
	s_lshl_b32 s32, s24, 19
	s_add_i32 s30, s30, s32
	s_lshl_b32 s32, s25, 8
	s_add_i32 s30, s30, s32
	s_lshl_b32 s31, s29, 11
	s_bfe_u32 s32, s25, 0x30001
	s_lshl_b32 s32, s32, 8
	s_add_i32 s31, s31, s32
	s_lshr_b32 s32, s25, 4
	s_lshl_b32 s32, s32, 7
	s_add_i32 s31, s31, s32
	s_and_b32 s32, s25, 1
	s_lshl_b32 s32, s32, 6
	s_add_i32 s31, s31, s32
	s_lshl_b32 s31, s31, 10
	s_lshl_b32 s32, s24, 6
	s_add_i32 s31, s31, s32
	s_add_i32 s31, s31, 0x2000000
	v_readlane_b32 s82, v239, 11
	v_readlane_b32 s83, v239, 12
	s_movk_i32 s97, 8192
	s_branch .Lp2w_go_b

.Lp2w_go_b:
	v_readlane_b32 s62, v239, 44
	v_readlane_b32 s63, v239, 45
	s_add_u32 s100, s82, s30
	s_addc_u32 s101, s83, 0
	s_add_u32 s70, s62, s31
	s_addc_u32 s71, s63, 0
	global_load_dword v34, v178, s[100:101] nt
	s_add_u32 s100, s100, s97
	s_addc_u32 s101, s101, 0
	global_load_dword v35, v178, s[100:101] nt
	s_add_u32 s100, s100, s97
	s_addc_u32 s101, s101, 0
	global_load_dword v36, v178, s[100:101] nt
	s_add_u32 s100, s100, s97
	s_addc_u32 s101, s101, 0
	global_load_dword v37, v178, s[100:101] nt
	s_add_u32 s100, s100, s97
	s_addc_u32 s101, s101, 0
	global_load_dword v38, v178, s[100:101] nt
	s_add_u32 s100, s100, s97
	s_addc_u32 s101, s101, 0
	global_load_dword v39, v178, s[100:101] nt
	s_add_u32 s100, s100, s97
	s_addc_u32 s101, s101, 0
	global_load_dword v40, v178, s[100:101] nt
	s_add_u32 s100, s100, s97
	s_addc_u32 s101, s101, 0
	global_load_dword v41, v178, s[100:101] nt
	s_add_u32 s100, s100, s97
	s_addc_u32 s101, s101, 0
	global_load_dword v42, v178, s[100:101] nt
	s_add_u32 s100, s100, s97
	s_addc_u32 s101, s101, 0
	global_load_dword v43, v178, s[100:101] nt
	s_add_u32 s100, s100, s97
	s_addc_u32 s101, s101, 0
	global_load_dword v44, v178, s[100:101] nt
	s_add_u32 s100, s100, s97
	s_addc_u32 s101, s101, 0
	global_load_dword v45, v178, s[100:101] nt
	s_add_u32 s100, s100, s97
	s_addc_u32 s101, s101, 0
	global_load_dword v46, v178, s[100:101] nt
	s_add_u32 s100, s100, s97
	s_addc_u32 s101, s101, 0
	global_load_dword v47, v178, s[100:101] nt
	s_add_u32 s100, s100, s97
	s_addc_u32 s101, s101, 0
	global_load_dword v48, v178, s[100:101] nt
	s_add_u32 s100, s100, s97
	s_addc_u32 s101, s101, 0
	global_load_dword v49, v178, s[100:101] nt
	s_add_u32 s100, s100, s97
	s_addc_u32 s101, s101, 0
	global_load_dword v50, v178, s[100:101] nt
	s_add_u32 s100, s100, s97
	s_addc_u32 s101, s101, 0
	global_load_dword v51, v178, s[100:101] nt
	s_add_u32 s100, s100, s97
	s_addc_u32 s101, s101, 0
	global_load_dword v52, v178, s[100:101] nt
	s_add_u32 s100, s100, s97
	s_addc_u32 s101, s101, 0
	global_load_dword v53, v178, s[100:101] nt
	s_add_u32 s100, s100, s97
	s_addc_u32 s101, s101, 0
	global_load_dword v54, v178, s[100:101] nt
	s_add_u32 s100, s100, s97
	s_addc_u32 s101, s101, 0
	global_load_dword v55, v178, s[100:101] nt
	s_add_u32 s100, s100, s97
	s_addc_u32 s101, s101, 0
	global_load_dword v56, v178, s[100:101] nt
	s_add_u32 s100, s100, s97
	s_addc_u32 s101, s101, 0
	global_load_dword v57, v178, s[100:101] nt
	s_add_u32 s100, s100, s97
	s_addc_u32 s101, s101, 0
	global_load_dword v58, v178, s[100:101] nt
	s_add_u32 s100, s100, s97
	s_addc_u32 s101, s101, 0
	global_load_dword v59, v178, s[100:101] nt
	s_add_u32 s100, s100, s97
	s_addc_u32 s101, s101, 0
	global_load_dword v60, v178, s[100:101] nt
	s_add_u32 s100, s100, s97
	s_addc_u32 s101, s101, 0
	global_load_dword v61, v178, s[100:101] nt
	s_add_u32 s100, s100, s97
	s_addc_u32 s101, s101, 0
	global_load_dword v62, v178, s[100:101] nt
	s_add_u32 s100, s100, s97
	s_addc_u32 s101, s101, 0
	global_load_dword v63, v178, s[100:101] nt
	s_add_u32 s100, s100, s97
	s_addc_u32 s101, s101, 0
	global_load_dword v64, v178, s[100:101] nt
	s_add_u32 s100, s100, s97
	s_addc_u32 s101, s101, 0
	global_load_dword v65, v178, s[100:101] nt
	s_add_u32 s100, s100, s97
	s_addc_u32 s101, s101, 0
	global_load_dword v66, v178, s[100:101] nt
	s_add_u32 s100, s100, s97
	s_addc_u32 s101, s101, 0
	global_load_dword v67, v178, s[100:101] nt
	s_add_u32 s100, s100, s97
	s_addc_u32 s101, s101, 0
	global_load_dword v68, v178, s[100:101] nt
	s_add_u32 s100, s100, s97
	s_addc_u32 s101, s101, 0
	global_load_dword v69, v178, s[100:101] nt
	s_add_u32 s100, s100, s97
	s_addc_u32 s101, s101, 0
	global_load_dword v70, v178, s[100:101] nt
	s_add_u32 s100, s100, s97
	s_addc_u32 s101, s101, 0
	global_load_dword v71, v178, s[100:101] nt
	s_add_u32 s100, s100, s97
	s_addc_u32 s101, s101, 0
	global_load_dword v72, v178, s[100:101] nt
	s_add_u32 s100, s100, s97
	s_addc_u32 s101, s101, 0
	global_load_dword v73, v178, s[100:101] nt
	s_add_u32 s100, s100, s97
	s_addc_u32 s101, s101, 0
	global_load_dword v74, v178, s[100:101] nt
	s_add_u32 s100, s100, s97
	s_addc_u32 s101, s101, 0
	global_load_dword v75, v178, s[100:101] nt
	s_add_u32 s100, s100, s97
	s_addc_u32 s101, s101, 0
	global_load_dword v76, v178, s[100:101] nt
	s_add_u32 s100, s100, s97
	s_addc_u32 s101, s101, 0
	global_load_dword v77, v178, s[100:101] nt
	s_add_u32 s100, s100, s97
	s_addc_u32 s101, s101, 0
	global_load_dword v78, v178, s[100:101] nt
	s_add_u32 s100, s100, s97
	s_addc_u32 s101, s101, 0
	global_load_dword v79, v178, s[100:101] nt
	s_add_u32 s100, s100, s97
	s_addc_u32 s101, s101, 0
	global_load_dword v80, v178, s[100:101] nt
	s_add_u32 s100, s100, s97
	s_addc_u32 s101, s101, 0
	global_load_dword v81, v178, s[100:101] nt
	s_add_u32 s100, s100, s97
	s_addc_u32 s101, s101, 0
	s_waitcnt vmcnt(32)
	v_mul_f32_e32 v34, 0x42000000, v34
	v_mul_f32_e32 v35, 0x42000000, v35
	v_mul_f32_e32 v36, 0x42000000, v36
	v_mul_f32_e32 v37, 0x42000000, v37
	v_mul_f32_e32 v38, 0x42000000, v38
	v_mul_f32_e32 v39, 0x42000000, v39
	v_mul_f32_e32 v40, 0x42000000, v40
	v_mul_f32_e32 v41, 0x42000000, v41
	v_mul_f32_e32 v42, 0x42000000, v42
	v_mul_f32_e32 v43, 0x42000000, v43
	v_mul_f32_e32 v44, 0x42000000, v44
	v_mul_f32_e32 v45, 0x42000000, v45
	v_mul_f32_e32 v46, 0x42000000, v46
	v_mul_f32_e32 v47, 0x42000000, v47
	v_mul_f32_e32 v48, 0x42000000, v48
	v_mul_f32_e32 v49, 0x42000000, v49
	v_cvt_pk_fp8_f32 v154, v34, v35
	v_cvt_pk_fp8_f32 v155, v38, v39
	v_cvt_pk_fp8_f32 v156, v42, v43
	v_cvt_pk_fp8_f32 v157, v46, v47
	v_cvt_pk_fp8_f32 v154, v36, v37 op_sel:[0,0,1]
	v_cvt_pk_fp8_f32 v155, v40, v41 op_sel:[0,0,1]
	v_cvt_pk_fp8_f32 v156, v44, v45 op_sel:[0,0,1]
	v_cvt_pk_fp8_f32 v157, v48, v49 op_sel:[0,0,1]
	global_load_dword v82, v178, s[100:101] nt
	s_add_u32 s100, s100, s97
	s_addc_u32 s101, s101, 0
	global_load_dword v83, v178, s[100:101] nt
	s_add_u32 s100, s100, s97
	s_addc_u32 s101, s101, 0
	global_load_dword v84, v178, s[100:101] nt
	s_add_u32 s100, s100, s97
	s_addc_u32 s101, s101, 0
	global_load_dword v85, v178, s[100:101] nt
	s_add_u32 s100, s100, s97
	s_addc_u32 s101, s101, 0
	global_load_dword v86, v178, s[100:101] nt
	s_add_u32 s100, s100, s97
	s_addc_u32 s101, s101, 0
	global_load_dword v87, v178, s[100:101] nt
	s_add_u32 s100, s100, s97
	s_addc_u32 s101, s101, 0
	global_load_dword v88, v178, s[100:101] nt
	s_add_u32 s100, s100, s97
	s_addc_u32 s101, s101, 0
	global_load_dword v89, v178, s[100:101] nt
	s_add_u32 s100, s100, s97
	s_addc_u32 s101, s101, 0
	global_load_dword v90, v178, s[100:101] nt
	s_add_u32 s100, s100, s97
	s_addc_u32 s101, s101, 0
	global_load_dword v91, v178, s[100:101] nt
	s_add_u32 s100, s100, s97
	s_addc_u32 s101, s101, 0
	global_load_dword v92, v178, s[100:101] nt
	s_add_u32 s100, s100, s97
	s_addc_u32 s101, s101, 0
	global_load_dword v93, v178, s[100:101] nt
	s_add_u32 s100, s100, s97
	s_addc_u32 s101, s101, 0
	global_load_dword v94, v178, s[100:101] nt
	s_add_u32 s100, s100, s97
	s_addc_u32 s101, s101, 0
	global_load_dword v95, v178, s[100:101] nt
	s_add_u32 s100, s100, s97
	s_addc_u32 s101, s101, 0
	global_load_dword v96, v178, s[100:101] nt
	s_add_u32 s100, s100, s97
	s_addc_u32 s101, s101, 0
	global_load_dword v97, v178, s[100:101] nt
	s_add_u32 s100, s100, s97
	s_addc_u32 s101, s101, 0
	s_waitcnt vmcnt(32)
	v_mul_f32_e32 v50, 0x42000000, v50
	v_mul_f32_e32 v51, 0x42000000, v51
	v_mul_f32_e32 v52, 0x42000000, v52
	v_mul_f32_e32 v53, 0x42000000, v53
	v_mul_f32_e32 v54, 0x42000000, v54
	v_mul_f32_e32 v55, 0x42000000, v55
	v_mul_f32_e32 v56, 0x42000000, v56
	v_mul_f32_e32 v57, 0x42000000, v57
	v_mul_f32_e32 v58, 0x42000000, v58
	v_mul_f32_e32 v59, 0x42000000, v59
	v_mul_f32_e32 v60, 0x42000000, v60
	v_mul_f32_e32 v61, 0x42000000, v61
	v_mul_f32_e32 v62, 0x42000000, v62
	v_mul_f32_e32 v63, 0x42000000, v63
	v_mul_f32_e32 v64, 0x42000000, v64
	v_mul_f32_e32 v65, 0x42000000, v65
	v_cvt_pk_fp8_f32 v158, v50, v51
	v_cvt_pk_fp8_f32 v159, v54, v55
	v_cvt_pk_fp8_f32 v160, v58, v59
	v_cvt_pk_fp8_f32 v161, v62, v63
	v_cvt_pk_fp8_f32 v158, v52, v53 op_sel:[0,0,1]
	v_cvt_pk_fp8_f32 v159, v56, v57 op_sel:[0,0,1]
	v_cvt_pk_fp8_f32 v160, v60, v61 op_sel:[0,0,1]
	v_cvt_pk_fp8_f32 v161, v64, v65 op_sel:[0,0,1]
	s_waitcnt vmcnt(16)
	v_mul_f32_e32 v66, 0x42000000, v66
	v_mul_f32_e32 v67, 0x42000000, v67
	v_mul_f32_e32 v68, 0x42000000, v68
	v_mul_f32_e32 v69, 0x42000000, v69
	v_mul_f32_e32 v70, 0x42000000, v70
	v_mul_f32_e32 v71, 0x42000000, v71
	v_mul_f32_e32 v72, 0x42000000, v72
	v_mul_f32_e32 v73, 0x42000000, v73
	v_mul_f32_e32 v74, 0x42000000, v74
	v_mul_f32_e32 v75, 0x42000000, v75
	v_mul_f32_e32 v76, 0x42000000, v76
	v_mul_f32_e32 v77, 0x42000000, v77
	v_mul_f32_e32 v78, 0x42000000, v78
	v_mul_f32_e32 v79, 0x42000000, v79
	v_mul_f32_e32 v80, 0x42000000, v80
	v_mul_f32_e32 v81, 0x42000000, v81
	v_cvt_pk_fp8_f32 v162, v66, v67
	v_cvt_pk_fp8_f32 v163, v70, v71
	v_cvt_pk_fp8_f32 v164, v74, v75
	v_cvt_pk_fp8_f32 v165, v78, v79
	v_cvt_pk_fp8_f32 v162, v68, v69 op_sel:[0,0,1]
	v_cvt_pk_fp8_f32 v163, v72, v73 op_sel:[0,0,1]
	v_cvt_pk_fp8_f32 v164, v76, v77 op_sel:[0,0,1]
	v_cvt_pk_fp8_f32 v165, v80, v81 op_sel:[0,0,1]
	s_waitcnt vmcnt(0)
	v_mul_f32_e32 v82, 0x42000000, v82
	v_mul_f32_e32 v83, 0x42000000, v83
	v_mul_f32_e32 v84, 0x42000000, v84
	v_mul_f32_e32 v85, 0x42000000, v85
	v_mul_f32_e32 v86, 0x42000000, v86
	v_mul_f32_e32 v87, 0x42000000, v87
	v_mul_f32_e32 v88, 0x42000000, v88
	v_mul_f32_e32 v89, 0x42000000, v89
	v_mul_f32_e32 v90, 0x42000000, v90
	v_mul_f32_e32 v91, 0x42000000, v91
	v_mul_f32_e32 v92, 0x42000000, v92
	v_mul_f32_e32 v93, 0x42000000, v93
	v_mul_f32_e32 v94, 0x42000000, v94
	v_mul_f32_e32 v95, 0x42000000, v95
	v_mul_f32_e32 v96, 0x42000000, v96
	v_mul_f32_e32 v97, 0x42000000, v97
	v_cvt_pk_fp8_f32 v166, v82, v83
	v_cvt_pk_fp8_f32 v167, v86, v87
	v_cvt_pk_fp8_f32 v168, v90, v91
	v_cvt_pk_fp8_f32 v169, v94, v95
	v_cvt_pk_fp8_f32 v166, v84, v85 op_sel:[0,0,1]
	v_cvt_pk_fp8_f32 v167, v88, v89 op_sel:[0,0,1]
	v_cvt_pk_fp8_f32 v168, v92, v93 op_sel:[0,0,1]
	v_cvt_pk_fp8_f32 v169, v96, v97 op_sel:[0,0,1]
	s_mov_b32 vcc_lo, 0xaaaaaaaa
	s_mov_b32 vcc_hi, 0xaaaaaaaa
	s_nop 1
	v_cndmask_b32_dpp v170, v154, v158, vcc quad_perm:[1,0,3,2] row_mask:0xf bank_mask:0xf
	v_cndmask_b32_dpp v174, v162, v166, vcc quad_perm:[1,0,3,2] row_mask:0xf bank_mask:0xf
	v_cndmask_b32_dpp v171, v155, v159, vcc quad_perm:[1,0,3,2] row_mask:0xf bank_mask:0xf
	v_cndmask_b32_dpp v175, v163, v167, vcc quad_perm:[1,0,3,2] row_mask:0xf bank_mask:0xf
	v_cndmask_b32_dpp v172, v156, v160, vcc quad_perm:[1,0,3,2] row_mask:0xf bank_mask:0xf
	v_cndmask_b32_dpp v176, v164, v168, vcc quad_perm:[1,0,3,2] row_mask:0xf bank_mask:0xf
	v_cndmask_b32_dpp v173, v157, v161, vcc quad_perm:[1,0,3,2] row_mask:0xf bank_mask:0xf
	v_cndmask_b32_dpp v177, v165, v169, vcc quad_perm:[1,0,3,2] row_mask:0xf bank_mask:0xf
	s_mov_b32 vcc_lo, 0x55555555
	s_mov_b32 vcc_hi, 0x55555555
	s_nop 1
	v_cndmask_b32_dpp v154, v158, v154, vcc quad_perm:[1,0,3,2] row_mask:0xf bank_mask:0xf
	v_cndmask_b32_dpp v162, v166, v162, vcc quad_perm:[1,0,3,2] row_mask:0xf bank_mask:0xf
	v_cndmask_b32_dpp v155, v159, v155, vcc quad_perm:[1,0,3,2] row_mask:0xf bank_mask:0xf
	v_cndmask_b32_dpp v163, v167, v163, vcc quad_perm:[1,0,3,2] row_mask:0xf bank_mask:0xf
	v_cndmask_b32_dpp v156, v160, v156, vcc quad_perm:[1,0,3,2] row_mask:0xf bank_mask:0xf
	v_cndmask_b32_dpp v164, v168, v164, vcc quad_perm:[1,0,3,2] row_mask:0xf bank_mask:0xf
	v_cndmask_b32_dpp v157, v161, v157, vcc quad_perm:[1,0,3,2] row_mask:0xf bank_mask:0xf
	v_cndmask_b32_dpp v165, v169, v165, vcc quad_perm:[1,0,3,2] row_mask:0xf bank_mask:0xf
	s_mov_b32 vcc_lo, 0xcccccccc
	s_mov_b32 vcc_hi, 0xcccccccc
	s_nop 1
	v_cndmask_b32_dpp v158, v154, v162, vcc quad_perm:[2,3,0,1] row_mask:0xf bank_mask:0xf
	v_cndmask_b32_dpp v166, v170, v174, vcc quad_perm:[2,3,0,1] row_mask:0xf bank_mask:0xf
	v_cndmask_b32_dpp v159, v155, v163, vcc quad_perm:[2,3,0,1] row_mask:0xf bank_mask:0xf
	v_cndmask_b32_dpp v167, v171, v175, vcc quad_perm:[2,3,0,1] row_mask:0xf bank_mask:0xf
	v_cndmask_b32_dpp v160, v156, v164, vcc quad_perm:[2,3,0,1] row_mask:0xf bank_mask:0xf
	v_cndmask_b32_dpp v168, v172, v176, vcc quad_perm:[2,3,0,1] row_mask:0xf bank_mask:0xf
	v_cndmask_b32_dpp v161, v157, v165, vcc quad_perm:[2,3,0,1] row_mask:0xf bank_mask:0xf
	v_cndmask_b32_dpp v169, v173, v177, vcc quad_perm:[2,3,0,1] row_mask:0xf bank_mask:0xf
	s_mov_b32 vcc_lo, 0x33333333
	s_mov_b32 vcc_hi, 0x33333333
	s_nop 1
	v_cndmask_b32_dpp v154, v162, v154, vcc quad_perm:[2,3,0,1] row_mask:0xf bank_mask:0xf
	v_cndmask_b32_dpp v170, v174, v170, vcc quad_perm:[2,3,0,1] row_mask:0xf bank_mask:0xf
	v_cndmask_b32_dpp v155, v163, v155, vcc quad_perm:[2,3,0,1] row_mask:0xf bank_mask:0xf
	v_cndmask_b32_dpp v171, v175, v171, vcc quad_perm:[2,3,0,1] row_mask:0xf bank_mask:0xf
	v_cndmask_b32_dpp v156, v164, v156, vcc quad_perm:[2,3,0,1] row_mask:0xf bank_mask:0xf
	v_cndmask_b32_dpp v172, v176, v172, vcc quad_perm:[2,3,0,1] row_mask:0xf bank_mask:0xf
	v_cndmask_b32_dpp v157, v165, v157, vcc quad_perm:[2,3,0,1] row_mask:0xf bank_mask:0xf
	v_cndmask_b32_dpp v173, v177, v173, vcc quad_perm:[2,3,0,1] row_mask:0xf bank_mask:0xf
	global_store_dwordx4 v179, v[154:157], s[70:71] nt
	global_store_dwordx4 v180, v[170:173], s[70:71] nt
	global_store_dwordx4 v181, v[158:161], s[70:71] nt
	global_store_dwordx4 v190, v[166:169], s[70:71] nt
	s_lshl_b32 s23, s74, 3
	s_add_i32 s98, s98, s23
	s_branch .Lp2w_tail

	.amdhsa_kernel _Z6mk_fwd4Args
		.amdhsa_group_segment_fixed_size 0
		.amdhsa_private_segment_fixed_size 0
		.amdhsa_kernarg_size 416
		.amdhsa_user_sgpr_count 2
		.amdhsa_user_sgpr_dispatch_ptr 0
		.amdhsa_user_sgpr_queue_ptr 0
		.amdhsa_user_sgpr_kernarg_segment_ptr 1
		.amdhsa_user_sgpr_dispatch_id 0
		.amdhsa_user_sgpr_kernarg_preload_length 0
		.amdhsa_user_sgpr_kernarg_preload_offset 0
		.amdhsa_user_sgpr_private_segment_size 0
		.amdhsa_uses_dynamic_stack 0
		.amdhsa_enable_private_segment 0
		.amdhsa_system_sgpr_workgroup_id_x 1
		.amdhsa_system_sgpr_workgroup_id_y 0
		.amdhsa_system_sgpr_workgroup_id_z 0
		.amdhsa_system_sgpr_workgroup_info 0
		.amdhsa_system_vgpr_workitem_id 0
		.amdhsa_next_free_vgpr 240
		.amdhsa_next_free_sgpr 102
		.amdhsa_accum_offset 240
		.amdhsa_reserve_vcc 1
		.amdhsa_float_round_mode_32 0
		.amdhsa_float_round_mode_16_64 0
		.amdhsa_float_denorm_mode_32 3
		.amdhsa_float_denorm_mode_16_64 3
		.amdhsa_dx10_clamp 1
		.amdhsa_ieee_mode 1
		.amdhsa_fp16_overflow 0
		.amdhsa_tg_split 0
		.amdhsa_exception_fp_ieee_invalid_op 0
		.amdhsa_exception_fp_denorm_src 0
		.amdhsa_exception_fp_ieee_div_zero 0
		.amdhsa_exception_fp_ieee_overflow 0
		.amdhsa_exception_fp_ieee_underflow 0
		.amdhsa_exception_fp_ieee_inexact 0
		.amdhsa_exception_int_div_zero 0
	.end_amdhsa_kernel

amdhsa.kernels:
  - .agpr_count:     0
    .args:
      - .offset:         0
        .size:           160
        .value_kind:     by_value
      - .offset:         160
        .size:           4
        .value_kind:     hidden_block_count_x
      - .offset:         164
        .size:           4
        .value_kind:     hidden_block_count_y
      - .offset:         168
        .size:           4
        .value_kind:     hidden_block_count_z
      - .offset:         172
        .size:           2
        .value_kind:     hidden_group_size_x
      - .offset:         174
        .size:           2
        .value_kind:     hidden_group_size_y
      - .offset:         176
        .size:           2
        .value_kind:     hidden_group_size_z
      - .offset:         178
        .size:           2
        .value_kind:     hidden_remainder_x
      - .offset:         180
        .size:           2
        .value_kind:     hidden_remainder_y
      - .offset:         182
        .size:           2
        .value_kind:     hidden_remainder_z
      - .offset:         200
        .size:           8
        .value_kind:     hidden_global_offset_x
      - .offset:         208
        .size:           8
        .value_kind:     hidden_global_offset_y
      - .offset:         216
        .size:           8
        .value_kind:     hidden_global_offset_z
      - .offset:         224
        .size:           2
        .value_kind:     hidden_grid_dims
      - .offset:         280
        .size:           4
        .value_kind:     hidden_dynamic_lds_size
    .group_segment_fixed_size: 0
    .kernarg_segment_align: 8
    .kernarg_segment_size: 416
    .language:       OpenCL C
    .language_version:
      - 2
      - 0
    .max_flat_workgroup_size: 512
    .name:           _Z6mk_fwd4Args
    .private_segment_fixed_size: 0
    .sgpr_count:     108
    .sgpr_spill_count: 115
    .symbol:         _Z6mk_fwd4Args.kd
    .uniform_work_group_size: 1
    .uses_dynamic_stack: false
    .vgpr_count:     240
    .vgpr_spill_count: 0
    .wavefront_size: 64
